# speedup vs baseline: 1.0563x; 1.0140x over previous
_Z16bilateral_kernelPKfS0_Pf:
	s_load_dwordx2 s[4:5], s[0:1], 0x0
	s_load_dwordx2 s[8:9], s[0:1], 0x10
	s_and_b32 s0, s2, 7
	s_mulk_i32 s0, 0x60
	s_lshr_b32 s1, s2, 3
	s_add_i32 s1, s0, s1
	s_lshr_b32 s0, s1, 6
	s_lshl_b32 s1, s1, 3
	s_and_b32 s10, s1, 0x1c0
	s_lshl_b32 s1, s2, 3
	s_nop 0
	s_and_b32 s11, s1, 0x1c0
	s_mov_b32 s1, 0
	s_lshl_b64 s[2:3], s[0:1], 20
	s_mov_b32 s20, 0xc05dfbe6
	s_mov_b32 s21, 0xc05dfbe6
	s_mov_b32 s22, 0xc0a8390e
	s_mov_b32 s23, 0xc0a8390e
	s_mov_b32 s24, 0xc08211a7
	s_mov_b32 s25, 0xc08211a7
	s_mov_b32 s26, 0xc0bb4cc1
	s_mov_b32 s27, 0xc0bb4cc1
	s_mov_b32 s28, 0xc0f487dc
	s_mov_b32 s29, 0xc0f487dc
	s_mov_b32 s30, 0x3e0bd796
	s_mov_b32 s31, 0x3e0bd796
	s_mov_b32 s32, 0x3f45a90c
	s_mov_b32 s33, 0x3f45a90c
	s_mov_b32 s34, 0x3fa5c782
	s_mov_b32 s35, 0x3fa5c782
	v_and_b32_e32 v118, 15, v0
	v_lshrrev_b32_e32 v115, 2, v0
	v_lshl_or_b32 v113, v118, 2, s11
	v_and_or_b32 v117, v115, 60, s10
	v_min_u32_e32 v116, 0x1fa, v113
	v_sub_u32_e64 v115, v113, 2 clamp
	v_add_u32_e32 v116, 4, v116
	s_nop 0
	v_cmp_eq_u32_e64 s[16:17], 0, v118
	v_cmp_eq_u32_e32 vcc, 15, v118
	s_nop 1
	v_cndmask_b32_e64 v115, v116, v115, s[16:17]
	s_or_b64 vcc, s[16:17], vcc
	v_lshlrev_b32_e32 v115, 2, v115
	v_mov_b32_e32 v116, 0x7ff00000
	s_nop 0
	v_cndmask_b32_e32 v112, v116, v115, vcc
	s_movk_i32 s18, 0x1fc
	v_cmp_eq_u32_e32 vcc, 0, v113
	v_cmp_eq_u32_e64 s[16:17], s18, v113
	v_lshlrev_b32_e32 v113, 2, v113
	s_waitcnt lgkmcnt(0)
	s_add_u32 s4, s4, s2
	s_addc_u32 s5, s5, s3
	s_and_b32 s5, s5, 0xffff
	s_mov_b32 s6, 0x100000
	s_mov_b32 s7, 0x20000
	s_add_u32 s12, s8, s2
	s_addc_u32 s13, s9, s3
	s_and_b32 s13, s13, 0xffff
	s_mov_b32 s14, 0x100000
	s_mov_b32 s15, 0x20000
	v_sub_u32_e64 v115, v117, 2 clamp
	v_lshlrev_b32_e32 v115, 11, v115
	v_add_u32_e32 v116, v115, v112
	v_add_u32_e32 v115, v115, v113
	s_nop 0
	buffer_load_dwordx2 v[0:1], v116, s[4:7], 0 offen nt
	buffer_load_dwordx2 v[6:7], v116, s[4:7], 0 offen nt
	buffer_load_dwordx4 v[2:5], v115, s[4:7], 0 offen nt
	v_sub_u32_e64 v115, v117, 1 clamp
	v_lshlrev_b32_e32 v115, 11, v115
	v_add_u32_e32 v116, v115, v112
	v_add_u32_e32 v115, v115, v113
	s_nop 0
	buffer_load_dwordx2 v[8:9], v116, s[4:7], 0 offen nt
	buffer_load_dwordx2 v[14:15], v116, s[4:7], 0 offen nt
	buffer_load_dwordx4 v[10:13], v115, s[4:7], 0 offen nt
	v_lshlrev_b32_e32 v115, 11, v117
	v_add_u32_e32 v116, v115, v112
	v_add_u32_e32 v114, v115, v113
	s_nop 0
	v_add_u32_e32 v119, 0x1000, v114
	buffer_load_dwordx2 v[16:17], v116, s[4:7], 0 offen nt
	buffer_load_dwordx2 v[22:23], v116, s[4:7], 0 offen nt
	buffer_load_dwordx4 v[18:21], v114, s[4:7], 0 offen nt
	v_lshlrev_b32_e32 v115, 11, v117
	s_nop 0
	v_add_u32_e32 v115, 0x800, v115
	v_add_u32_e32 v116, v115, v112
	v_add_u32_e32 v115, v115, v113
	buffer_load_dwordx2 v[24:25], v116, s[4:7], 0 offen nt
	buffer_load_dwordx2 v[30:31], v116, s[4:7], 0 offen nt
	buffer_load_dwordx4 v[26:29], v115, s[4:7], 0 offen nt
	v_lshlrev_b32_e32 v115, 11, v117
	s_nop 0
	v_add_u32_e32 v115, 0x1000, v115
	v_add_u32_e32 v116, v115, v112
	v_add_u32_e32 v115, v115, v113
	buffer_load_dwordx2 v[32:33], v116, s[4:7], 0 offen nt
	buffer_load_dwordx2 v[38:39], v116, s[4:7], 0 offen nt
	buffer_load_dwordx4 v[34:37], v115, s[4:7], 0 offen nt
	v_lshlrev_b32_e32 v115, 11, v117
	s_nop 0
	v_add_u32_e32 v115, 0x1800, v115
	v_add_u32_e32 v116, v115, v112
	v_add_u32_e32 v115, v115, v113
	buffer_load_dwordx2 v[40:41], v116, s[4:7], 0 offen nt
	buffer_load_dwordx2 v[46:47], v116, s[4:7], 0 offen nt
	buffer_load_dwordx4 v[42:45], v115, s[4:7], 0 offen nt
	v_min_u32_e32 v115, 0x1fb, v117
	v_lshlrev_b32_e32 v115, 11, v115
	s_nop 0
	v_add_u32_e32 v115, 0x2000, v115
	v_add_u32_e32 v116, v115, v112
	v_add_u32_e32 v115, v115, v113
	buffer_load_dwordx2 v[48:49], v116, s[4:7], 0 offen nt
	buffer_load_dwordx2 v[54:55], v116, s[4:7], 0 offen nt
	buffer_load_dwordx4 v[50:53], v115, s[4:7], 0 offen nt
	v_min_u32_e32 v115, 0x1fa, v117
	v_lshlrev_b32_e32 v115, 11, v115
	s_nop 0
	v_add_u32_e32 v115, 0x2800, v115
	v_add_u32_e32 v116, v115, v112
	v_add_u32_e32 v115, v115, v113
	buffer_load_dwordx2 v[56:57], v116, s[4:7], 0 offen nt
	buffer_load_dwordx2 v[62:63], v116, s[4:7], 0 offen nt
	buffer_load_dwordx4 v[58:61], v115, s[4:7], 0 offen nt
	s_waitcnt vmcnt(21)
	s_nop 0
	v_mov_b32_dpp v0, v4 row_shr:1 row_mask:0xf bank_mask:0xf
	v_mov_b32_dpp v1, v5 row_shr:1 row_mask:0xf bank_mask:0xf
	v_mov_b32_dpp v6, v2 row_shl:1 row_mask:0xf bank_mask:0xf
	v_mov_b32_dpp v7, v3 row_shl:1 row_mask:0xf bank_mask:0xf
	v_pk_mul_f32 v[2:3], v[2:3], s[32:33]
	v_pk_mul_f32 v[4:5], v[4:5], s[32:33]
	v_cndmask_b32_e64 v1, v1, v0, vcc
	v_cndmask_b32_e64 v6, v6, v7, s[16:17]
	v_pk_mul_f32 v[0:1], v[0:1], s[32:33]
	v_pk_mul_f32 v[6:7], v[6:7], s[32:33]
	s_waitcnt vmcnt(18)
	s_nop 0
	v_mov_b32_dpp v8, v12 row_shr:1 row_mask:0xf bank_mask:0xf
	v_mov_b32_dpp v9, v13 row_shr:1 row_mask:0xf bank_mask:0xf
	v_mov_b32_dpp v14, v10 row_shl:1 row_mask:0xf bank_mask:0xf
	v_mov_b32_dpp v15, v11 row_shl:1 row_mask:0xf bank_mask:0xf
	v_pk_mul_f32 v[10:11], v[10:11], s[32:33]
	v_pk_mul_f32 v[12:13], v[12:13], s[32:33]
	v_cndmask_b32_e64 v9, v9, v8, vcc
	v_cndmask_b32_e64 v14, v14, v15, s[16:17]
	v_pk_mul_f32 v[8:9], v[8:9], s[32:33]
	v_pk_mul_f32 v[14:15], v[14:15], s[32:33]
	s_waitcnt vmcnt(15)
	s_nop 0
	v_mov_b32_dpp v16, v20 row_shr:1 row_mask:0xf bank_mask:0xf
	v_mov_b32_dpp v17, v21 row_shr:1 row_mask:0xf bank_mask:0xf
	v_mov_b32_dpp v22, v18 row_shl:1 row_mask:0xf bank_mask:0xf
	v_mov_b32_dpp v23, v19 row_shl:1 row_mask:0xf bank_mask:0xf
	v_pk_mul_f32 v[18:19], v[18:19], s[32:33]
	v_pk_mul_f32 v[20:21], v[20:21], s[32:33]
	v_cndmask_b32_e64 v17, v17, v16, vcc
	v_cndmask_b32_e64 v22, v22, v23, s[16:17]
	v_pk_mul_f32 v[68:69], v[18:19], s[30:31]
	v_pk_mul_f32 v[70:71], v[20:21], s[30:31]
	v_pk_mul_f32 v[16:17], v[16:17], s[32:33]
	v_pk_mul_f32 v[22:23], v[22:23], s[32:33]
	v_mov_b32_e32 v64, s30
	v_mov_b32_e32 v65, s30
	v_mov_b32_e32 v66, s30
	v_mov_b32_e32 v67, s30
	s_setprio 3
	s_nop 0
	v_pk_add_f32 v[96:97], v[18:19], v[0:1] neg_lo:[0,1] neg_hi:[0,1]
	v_pk_add_f32 v[98:99], v[18:19], v[2:3] neg_lo:[0,1] neg_hi:[0,1]
	v_pk_add_f32 v[100:101], v[20:21], v[2:3] neg_lo:[0,1] neg_hi:[0,1]
	v_pk_add_f32 v[102:103], v[18:19], v[4:5] neg_lo:[0,1] neg_hi:[0,1]
	v_pk_fma_f32 v[96:97], v[96:97], v[96:97], s[28:29] neg_lo:[1,0,0] neg_hi:[1,0,0]
	v_pk_fma_f32 v[98:99], v[98:99], v[98:99], s[22:23] neg_lo:[1,0,0] neg_hi:[1,0,0]
	v_pk_fma_f32 v[100:101], v[100:101], v[100:101], s[28:29] neg_lo:[1,0,0] neg_hi:[1,0,0]
	v_pk_fma_f32 v[102:103], v[102:103], v[102:103], s[28:29] neg_lo:[1,0,0] neg_hi:[1,0,0]
	v_exp_f32_e32 v96, v96
	v_exp_f32_e32 v97, v97
	v_exp_f32_e32 v98, v98
	v_exp_f32_e32 v99, v99
	v_exp_f32_e32 v100, v100
	v_exp_f32_e32 v101, v101
	v_exp_f32_e32 v102, v102
	v_exp_f32_e32 v103, v103
	v_pk_add_f32 v[104:105], v[20:21], v[4:5] neg_lo:[0,1] neg_hi:[0,1]
	v_pk_add_f32 v[106:107], v[20:21], v[6:7] neg_lo:[0,1] neg_hi:[0,1]
	v_pk_add_f32 v[108:109], v[18:19], v[2:3] op_sel:[1,0] op_sel_hi:[0,1] neg_lo:[0,1] neg_hi:[0,1]
	v_pk_add_f32 v[110:111], v[20:21], v[4:5] op_sel:[1,0] op_sel_hi:[0,1] neg_lo:[0,1] neg_hi:[0,1]
	v_pk_fma_f32 v[104:105], v[104:105], v[104:105], s[22:23] neg_lo:[1,0,0] neg_hi:[1,0,0]
	v_pk_fma_f32 v[106:107], v[106:107], v[106:107], s[28:29] neg_lo:[1,0,0] neg_hi:[1,0,0]
	v_pk_fma_f32 v[108:109], v[108:109], v[108:109], s[26:27] neg_lo:[1,0,0] neg_hi:[1,0,0]
	v_pk_fma_f32 v[110:111], v[110:111], v[110:111], s[26:27] neg_lo:[1,0,0] neg_hi:[1,0,0]
	v_exp_f32_e32 v104, v104
	v_exp_f32_e32 v105, v105
	v_exp_f32_e32 v106, v106
	v_exp_f32_e32 v107, v107
	v_exp_f32_e32 v108, v108
	v_exp_f32_e32 v109, v109
	v_exp_f32_e32 v110, v110
	v_exp_f32_e32 v111, v111
	v_pk_add_f32 v[64:65], v[64:65], v[96:97]
	v_pk_fma_f32 v[68:69], v[96:97], v[0:1], v[68:69]
	v_pk_add_f32 v[66:67], v[66:67], v[100:101]
	v_pk_add_f32 v[64:65], v[64:65], v[98:99]
	v_pk_fma_f32 v[68:69], v[98:99], v[2:3], v[68:69]
	v_pk_fma_f32 v[70:71], v[100:101], v[2:3], v[70:71]
	v_pk_add_f32 v[64:65], v[64:65], v[102:103]
	v_pk_fma_f32 v[68:69], v[102:103], v[4:5], v[68:69]
	v_pk_add_f32 v[96:97], v[18:19], v[8:9] neg_lo:[0,1] neg_hi:[0,1]
	v_pk_add_f32 v[98:99], v[18:19], v[10:11] neg_lo:[0,1] neg_hi:[0,1]
	v_pk_add_f32 v[100:101], v[20:21], v[10:11] neg_lo:[0,1] neg_hi:[0,1]
	v_pk_add_f32 v[102:103], v[18:19], v[12:13] neg_lo:[0,1] neg_hi:[0,1]
	v_pk_fma_f32 v[96:97], v[96:97], v[96:97], s[26:27] neg_lo:[1,0,0] neg_hi:[1,0,0]
	v_pk_fma_f32 v[98:99], v[98:99], v[98:99], s[20:21] neg_lo:[1,0,0] neg_hi:[1,0,0]
	v_pk_fma_f32 v[100:101], v[100:101], v[100:101], s[26:27] neg_lo:[1,0,0] neg_hi:[1,0,0]
	v_pk_fma_f32 v[102:103], v[102:103], v[102:103], s[26:27] neg_lo:[1,0,0] neg_hi:[1,0,0]
	v_exp_f32_e32 v96, v96
	v_exp_f32_e32 v97, v97
	v_exp_f32_e32 v98, v98
	v_exp_f32_e32 v99, v99
	v_exp_f32_e32 v100, v100
	v_exp_f32_e32 v101, v101
	v_exp_f32_e32 v102, v102
	v_exp_f32_e32 v103, v103
	v_pk_add_f32 v[66:67], v[66:67], v[104:105]
	v_pk_fma_f32 v[70:71], v[104:105], v[4:5], v[70:71]
	v_pk_add_f32 v[64:65], v[64:65], v[108:109] op_sel:[0,1] op_sel_hi:[1,0]
	v_pk_add_f32 v[66:67], v[66:67], v[106:107]
	v_pk_fma_f32 v[70:71], v[106:107], v[6:7], v[70:71]
	v_pk_fma_f32 v[68:69], v[108:109], v[2:3], v[68:69] op_sel:[1,1,0] op_sel_hi:[0,0,1]
	v_pk_add_f32 v[66:67], v[66:67], v[110:111] op_sel:[0,1] op_sel_hi:[1,0]
	v_pk_fma_f32 v[70:71], v[110:111], v[4:5], v[70:71] op_sel:[1,1,0] op_sel_hi:[0,0,1]
	v_pk_add_f32 v[104:105], v[20:21], v[12:13] neg_lo:[0,1] neg_hi:[0,1]
	v_pk_add_f32 v[106:107], v[20:21], v[14:15] neg_lo:[0,1] neg_hi:[0,1]
	v_pk_add_f32 v[108:109], v[18:19], v[10:11] op_sel:[1,0] op_sel_hi:[0,1] neg_lo:[0,1] neg_hi:[0,1]
	v_pk_add_f32 v[110:111], v[20:21], v[12:13] op_sel:[1,0] op_sel_hi:[0,1] neg_lo:[0,1] neg_hi:[0,1]
	v_pk_fma_f32 v[104:105], v[104:105], v[104:105], s[20:21] neg_lo:[1,0,0] neg_hi:[1,0,0]
	v_pk_fma_f32 v[106:107], v[106:107], v[106:107], s[26:27] neg_lo:[1,0,0] neg_hi:[1,0,0]
	v_pk_fma_f32 v[108:109], v[108:109], v[108:109], s[24:25] neg_lo:[1,0,0] neg_hi:[1,0,0]
	v_pk_fma_f32 v[110:111], v[110:111], v[110:111], s[24:25] neg_lo:[1,0,0] neg_hi:[1,0,0]
	v_exp_f32_e32 v104, v104
	v_exp_f32_e32 v105, v105
	v_exp_f32_e32 v106, v106
	v_exp_f32_e32 v107, v107
	v_exp_f32_e32 v108, v108
	v_exp_f32_e32 v109, v109
	v_exp_f32_e32 v110, v110
	v_exp_f32_e32 v111, v111
	v_pk_add_f32 v[64:65], v[64:65], v[96:97]
	v_pk_fma_f32 v[68:69], v[96:97], v[8:9], v[68:69]
	v_pk_add_f32 v[66:67], v[66:67], v[100:101]
	v_pk_add_f32 v[64:65], v[64:65], v[98:99]
	v_pk_fma_f32 v[68:69], v[98:99], v[10:11], v[68:69]
	v_pk_fma_f32 v[70:71], v[100:101], v[10:11], v[70:71]
	v_pk_add_f32 v[64:65], v[64:65], v[102:103]
	v_pk_fma_f32 v[68:69], v[102:103], v[12:13], v[68:69]
	v_pk_add_f32 v[96:97], v[18:19], v[16:17] neg_lo:[0,1] neg_hi:[0,1]
	v_pk_add_f32 v[98:99], v[20:21], v[18:19] neg_lo:[0,1] neg_hi:[0,1]
	v_pk_add_f32 v[100:101], v[22:23], v[20:21] neg_lo:[0,1] neg_hi:[0,1]
	v_pk_fma_f32 v[96:97], v[96:97], v[96:97], s[22:23] neg_lo:[1,0,0] neg_hi:[1,0,0]
	v_pk_fma_f32 v[98:99], v[98:99], v[98:99], s[22:23] neg_lo:[1,0,0] neg_hi:[1,0,0]
	v_pk_fma_f32 v[100:101], v[100:101], v[100:101], s[22:23] neg_lo:[1,0,0] neg_hi:[1,0,0]
	v_exp_f32_e32 v96, v96
	v_exp_f32_e32 v97, v97
	v_exp_f32_e32 v98, v98
	v_exp_f32_e32 v99, v99
	v_exp_f32_e32 v100, v100
	v_exp_f32_e32 v101, v101
	v_pk_add_f32 v[66:67], v[66:67], v[104:105]
	v_pk_fma_f32 v[70:71], v[104:105], v[12:13], v[70:71]
	v_pk_add_f32 v[64:65], v[64:65], v[108:109] op_sel:[0,1] op_sel_hi:[1,0]
	v_pk_add_f32 v[66:67], v[66:67], v[106:107]
	v_pk_fma_f32 v[70:71], v[106:107], v[14:15], v[70:71]
	v_pk_fma_f32 v[68:69], v[108:109], v[10:11], v[68:69] op_sel:[1,1,0] op_sel_hi:[0,0,1]
	v_pk_add_f32 v[66:67], v[66:67], v[110:111] op_sel:[0,1] op_sel_hi:[1,0]
	v_pk_fma_f32 v[70:71], v[110:111], v[12:13], v[70:71] op_sel:[1,1,0] op_sel_hi:[0,0,1]
	v_sub_f32_e32 v104, v18, v1
	v_sub_f32_e32 v106, v20, v3
	v_sub_f32_e32 v108, v19, v4
	v_sub_f32_e32 v110, v21, v6
	v_sub_f32_e32 v105, v18, v9
	v_sub_f32_e32 v107, v20, v11
	v_sub_f32_e32 v109, v19, v12
	v_sub_f32_e32 v111, v21, v14
	v_fma_f32 v104, -v104, v104, s26
	v_fma_f32 v106, -v106, v106, s26
	v_fma_f32 v108, -v108, v108, s26
	v_fma_f32 v110, -v110, v110, s26
	v_fma_f32 v105, -v105, v105, s24
	v_fma_f32 v107, -v107, v107, s24
	v_fma_f32 v109, -v109, v109, s24
	v_fma_f32 v111, -v111, v111, s24
	v_exp_f32_e32 v104, v104
	v_exp_f32_e32 v106, v106
	v_exp_f32_e32 v108, v108
	v_exp_f32_e32 v110, v110
	v_exp_f32_e32 v105, v105
	v_exp_f32_e32 v107, v107
	v_exp_f32_e32 v109, v109
	v_exp_f32_e32 v111, v111
	v_pk_add_f32 v[64:65], v[64:65], v[96:97]
	v_pk_fma_f32 v[68:69], v[96:97], v[16:17], v[68:69]
	v_pk_add_f32 v[66:67], v[66:67], v[98:99]
	v_pk_add_f32 v[64:65], v[64:65], v[98:99]
	v_pk_fma_f32 v[68:69], v[98:99], v[20:21], v[68:69]
	v_pk_fma_f32 v[70:71], v[98:99], v[18:19], v[70:71]
	v_pk_add_f32 v[66:67], v[66:67], v[100:101]
	v_pk_fma_f32 v[70:71], v[100:101], v[22:23], v[70:71]
	v_sub_f32_e32 v100, v18, v17
	v_sub_f32_e32 v96, v19, v18
	v_sub_f32_e32 v102, v20, v19
	v_sub_f32_e32 v98, v21, v20
	v_sub_f32_e32 v97, v22, v21
	s_nop 0
	v_fma_f32 v100, -v100, v100, s20
	v_fma_f32 v96, -v96, v96, s20
	v_fma_f32 v102, -v102, v102, s20
	v_fma_f32 v98, -v98, v98, s20
	v_fma_f32 v97, -v97, v97, s20
	v_exp_f32_e32 v100, v100
	v_exp_f32_e32 v96, v96
	v_exp_f32_e32 v102, v102
	v_exp_f32_e32 v98, v98
	v_exp_f32_e32 v97, v97
	v_add_f32_e32 v64, v64, v104
	v_fmac_f32_e32 v68, v104, v1
	v_add_f32_e32 v66, v66, v106
	v_fmac_f32_e32 v70, v106, v3
	v_add_f32_e32 v65, v65, v108
	v_fmac_f32_e32 v69, v108, v4
	v_add_f32_e32 v67, v67, v110
	v_fmac_f32_e32 v71, v110, v6
	v_add_f32_e32 v64, v64, v105
	v_fmac_f32_e32 v68, v105, v9
	v_add_f32_e32 v66, v66, v107
	v_fmac_f32_e32 v70, v107, v11
	v_add_f32_e32 v65, v65, v109
	v_fmac_f32_e32 v69, v109, v12
	v_add_f32_e32 v67, v67, v111
	v_fmac_f32_e32 v71, v111, v14
	v_add_f32_e32 v64, v64, v100
	v_fmac_f32_e32 v68, v100, v17
	v_add_f32_e32 v65, v65, v102
	v_fmac_f32_e32 v69, v102, v20
	v_add_f32_e32 v66, v66, v102
	v_fmac_f32_e32 v70, v102, v19
	v_add_f32_e32 v67, v67, v97
	v_fmac_f32_e32 v71, v97, v22
	s_nop 0
	v_pk_add_f32 v[64:65], v[64:65], v[96:97] op_sel_hi:[1,0]
	v_pk_fma_f32 v[68:69], v[96:97], v[18:19], v[68:69] op_sel:[0,1,0] op_sel_hi:[0,0,1]
	v_pk_add_f32 v[66:67], v[66:67], v[98:99] op_sel_hi:[1,0]
	v_pk_fma_f32 v[70:71], v[98:99], v[20:21], v[70:71] op_sel:[0,1,0] op_sel_hi:[0,0,1]
	s_waitcnt vmcnt(12)
	s_nop 0
	v_mov_b32_dpp v24, v28 row_shr:1 row_mask:0xf bank_mask:0xf
	v_mov_b32_dpp v25, v29 row_shr:1 row_mask:0xf bank_mask:0xf
	v_mov_b32_dpp v30, v26 row_shl:1 row_mask:0xf bank_mask:0xf
	v_mov_b32_dpp v31, v27 row_shl:1 row_mask:0xf bank_mask:0xf
	v_pk_mul_f32 v[26:27], v[26:27], s[32:33]
	v_pk_mul_f32 v[28:29], v[28:29], s[32:33]
	v_cndmask_b32_e64 v25, v25, v24, vcc
	v_cndmask_b32_e64 v30, v30, v31, s[16:17]
	v_pk_mul_f32 v[76:77], v[26:27], s[30:31]
	v_pk_mul_f32 v[78:79], v[28:29], s[30:31]
	v_pk_mul_f32 v[24:25], v[24:25], s[32:33]
	v_pk_mul_f32 v[30:31], v[30:31], s[32:33]
	v_mov_b32_e32 v72, s30
	v_mov_b32_e32 v73, s30
	v_mov_b32_e32 v74, s30
	v_mov_b32_e32 v75, s30
	s_setprio 3
	s_nop 0
	v_pk_add_f32 v[96:97], v[26:27], v[8:9] neg_lo:[0,1] neg_hi:[0,1]
	v_pk_add_f32 v[98:99], v[26:27], v[10:11] neg_lo:[0,1] neg_hi:[0,1]
	v_pk_add_f32 v[100:101], v[28:29], v[10:11] neg_lo:[0,1] neg_hi:[0,1]
	v_pk_add_f32 v[102:103], v[26:27], v[12:13] neg_lo:[0,1] neg_hi:[0,1]
	v_pk_fma_f32 v[96:97], v[96:97], v[96:97], s[28:29] neg_lo:[1,0,0] neg_hi:[1,0,0]
	v_pk_fma_f32 v[98:99], v[98:99], v[98:99], s[22:23] neg_lo:[1,0,0] neg_hi:[1,0,0]
	v_pk_fma_f32 v[100:101], v[100:101], v[100:101], s[28:29] neg_lo:[1,0,0] neg_hi:[1,0,0]
	v_pk_fma_f32 v[102:103], v[102:103], v[102:103], s[28:29] neg_lo:[1,0,0] neg_hi:[1,0,0]
	v_exp_f32_e32 v96, v96
	v_exp_f32_e32 v97, v97
	v_exp_f32_e32 v98, v98
	v_exp_f32_e32 v99, v99
	v_exp_f32_e32 v100, v100
	v_exp_f32_e32 v101, v101
	v_exp_f32_e32 v102, v102
	v_exp_f32_e32 v103, v103
	v_pk_add_f32 v[104:105], v[28:29], v[12:13] neg_lo:[0,1] neg_hi:[0,1]
	v_pk_add_f32 v[106:107], v[28:29], v[14:15] neg_lo:[0,1] neg_hi:[0,1]
	v_pk_add_f32 v[108:109], v[26:27], v[10:11] op_sel:[1,0] op_sel_hi:[0,1] neg_lo:[0,1] neg_hi:[0,1]
	v_pk_add_f32 v[110:111], v[28:29], v[12:13] op_sel:[1,0] op_sel_hi:[0,1] neg_lo:[0,1] neg_hi:[0,1]
	v_pk_fma_f32 v[104:105], v[104:105], v[104:105], s[22:23] neg_lo:[1,0,0] neg_hi:[1,0,0]
	v_pk_fma_f32 v[106:107], v[106:107], v[106:107], s[28:29] neg_lo:[1,0,0] neg_hi:[1,0,0]
	v_pk_fma_f32 v[108:109], v[108:109], v[108:109], s[26:27] neg_lo:[1,0,0] neg_hi:[1,0,0]
	v_pk_fma_f32 v[110:111], v[110:111], v[110:111], s[26:27] neg_lo:[1,0,0] neg_hi:[1,0,0]
	v_exp_f32_e32 v104, v104
	v_exp_f32_e32 v105, v105
	v_exp_f32_e32 v106, v106
	v_exp_f32_e32 v107, v107
	v_exp_f32_e32 v108, v108
	v_exp_f32_e32 v109, v109
	v_exp_f32_e32 v110, v110
	v_exp_f32_e32 v111, v111
	v_pk_add_f32 v[72:73], v[72:73], v[96:97]
	v_pk_fma_f32 v[76:77], v[96:97], v[8:9], v[76:77]
	v_pk_add_f32 v[74:75], v[74:75], v[100:101]
	v_pk_add_f32 v[72:73], v[72:73], v[98:99]
	v_pk_fma_f32 v[76:77], v[98:99], v[10:11], v[76:77]
	v_pk_fma_f32 v[78:79], v[100:101], v[10:11], v[78:79]
	v_pk_add_f32 v[72:73], v[72:73], v[102:103]
	v_pk_fma_f32 v[76:77], v[102:103], v[12:13], v[76:77]
	v_pk_add_f32 v[96:97], v[26:27], v[16:17] neg_lo:[0,1] neg_hi:[0,1]
	v_pk_add_f32 v[98:99], v[24:25], v[18:19] neg_lo:[0,1] neg_hi:[0,1]
	v_pk_add_f32 v[100:101], v[26:27], v[18:19] neg_lo:[0,1] neg_hi:[0,1]
	v_pk_add_f32 v[102:103], v[28:29], v[18:19] neg_lo:[0,1] neg_hi:[0,1]
	v_pk_fma_f32 v[96:97], v[96:97], v[96:97], s[26:27] neg_lo:[1,0,0] neg_hi:[1,0,0]
	v_pk_fma_f32 v[98:99], v[98:99], v[98:99], s[26:27] neg_lo:[1,0,0] neg_hi:[1,0,0]
	v_pk_fma_f32 v[100:101], v[100:101], v[100:101], s[20:21] neg_lo:[1,0,0] neg_hi:[1,0,0]
	v_pk_fma_f32 v[102:103], v[102:103], v[102:103], s[26:27] neg_lo:[1,0,0] neg_hi:[1,0,0]
	v_exp_f32_e32 v96, v96
	v_exp_f32_e32 v97, v97
	v_exp_f32_e32 v98, v98
	v_exp_f32_e32 v99, v99
	v_exp_f32_e32 v100, v100
	v_exp_f32_e32 v101, v101
	v_exp_f32_e32 v102, v102
	v_exp_f32_e32 v103, v103
	v_pk_add_f32 v[74:75], v[74:75], v[104:105]
	v_pk_fma_f32 v[78:79], v[104:105], v[12:13], v[78:79]
	v_pk_add_f32 v[72:73], v[72:73], v[108:109] op_sel:[0,1] op_sel_hi:[1,0]
	v_pk_add_f32 v[74:75], v[74:75], v[106:107]
	v_pk_fma_f32 v[78:79], v[106:107], v[14:15], v[78:79]
	v_pk_fma_f32 v[76:77], v[108:109], v[10:11], v[76:77] op_sel:[1,1,0] op_sel_hi:[0,0,1]
	v_pk_add_f32 v[74:75], v[74:75], v[110:111] op_sel:[0,1] op_sel_hi:[1,0]
	v_pk_fma_f32 v[78:79], v[110:111], v[12:13], v[78:79] op_sel:[1,1,0] op_sel_hi:[0,0,1]
	v_pk_add_f32 v[104:105], v[26:27], v[20:21] neg_lo:[0,1] neg_hi:[0,1]
	v_pk_add_f32 v[106:107], v[28:29], v[20:21] neg_lo:[0,1] neg_hi:[0,1]
	v_pk_add_f32 v[108:109], v[30:31], v[20:21] neg_lo:[0,1] neg_hi:[0,1]
	v_pk_add_f32 v[110:111], v[28:29], v[22:23] neg_lo:[0,1] neg_hi:[0,1]
	v_pk_fma_f32 v[104:105], v[104:105], v[104:105], s[26:27] neg_lo:[1,0,0] neg_hi:[1,0,0]
	v_pk_fma_f32 v[106:107], v[106:107], v[106:107], s[20:21] neg_lo:[1,0,0] neg_hi:[1,0,0]
	v_pk_fma_f32 v[108:109], v[108:109], v[108:109], s[26:27] neg_lo:[1,0,0] neg_hi:[1,0,0]
	v_pk_fma_f32 v[110:111], v[110:111], v[110:111], s[26:27] neg_lo:[1,0,0] neg_hi:[1,0,0]
	v_exp_f32_e32 v104, v104
	v_exp_f32_e32 v105, v105
	v_exp_f32_e32 v106, v106
	v_exp_f32_e32 v107, v107
	v_exp_f32_e32 v108, v108
	v_exp_f32_e32 v109, v109
	v_exp_f32_e32 v110, v110
	v_exp_f32_e32 v111, v111
	v_pk_add_f32 v[72:73], v[72:73], v[96:97]
	v_pk_fma_f32 v[76:77], v[96:97], v[16:17], v[76:77]
	v_pk_add_f32 v[64:65], v[64:65], v[98:99]
	v_pk_fma_f32 v[68:69], v[98:99], v[24:25], v[68:69]
	v_pk_add_f32 v[72:73], v[72:73], v[100:101]
	v_pk_add_f32 v[64:65], v[64:65], v[100:101]
	v_pk_fma_f32 v[68:69], v[100:101], v[26:27], v[68:69]
	v_pk_fma_f32 v[76:77], v[100:101], v[18:19], v[76:77]
	v_pk_add_f32 v[64:65], v[64:65], v[102:103]
	v_pk_fma_f32 v[68:69], v[102:103], v[28:29], v[68:69]
	v_pk_add_f32 v[74:75], v[74:75], v[102:103]
	v_pk_fma_f32 v[78:79], v[102:103], v[18:19], v[78:79]
	v_pk_add_f32 v[96:97], v[26:27], v[18:19] op_sel:[1,0] op_sel_hi:[0,1] neg_lo:[0,1] neg_hi:[0,1]
	v_pk_add_f32 v[98:99], v[28:29], v[20:21] op_sel:[1,0] op_sel_hi:[0,1] neg_lo:[0,1] neg_hi:[0,1]
	v_pk_add_f32 v[100:101], v[26:27], v[24:25] neg_lo:[0,1] neg_hi:[0,1]
	v_pk_add_f32 v[102:103], v[28:29], v[26:27] neg_lo:[0,1] neg_hi:[0,1]
	v_pk_fma_f32 v[96:97], v[96:97], v[96:97], s[24:25] neg_lo:[1,0,0] neg_hi:[1,0,0]
	v_pk_fma_f32 v[98:99], v[98:99], v[98:99], s[24:25] neg_lo:[1,0,0] neg_hi:[1,0,0]
	v_pk_fma_f32 v[100:101], v[100:101], v[100:101], s[22:23] neg_lo:[1,0,0] neg_hi:[1,0,0]
	v_pk_fma_f32 v[102:103], v[102:103], v[102:103], s[22:23] neg_lo:[1,0,0] neg_hi:[1,0,0]
	v_exp_f32_e32 v96, v96
	v_exp_f32_e32 v97, v97
	v_exp_f32_e32 v98, v98
	v_exp_f32_e32 v99, v99
	v_exp_f32_e32 v100, v100
	v_exp_f32_e32 v101, v101
	v_exp_f32_e32 v102, v102
	v_exp_f32_e32 v103, v103
	v_pk_add_f32 v[66:67], v[66:67], v[104:105]
	v_pk_fma_f32 v[70:71], v[104:105], v[26:27], v[70:71]
	v_pk_add_f32 v[72:73], v[72:73], v[104:105]
	v_pk_fma_f32 v[76:77], v[104:105], v[20:21], v[76:77]
	v_pk_add_f32 v[66:67], v[66:67], v[106:107]
	v_pk_fma_f32 v[70:71], v[106:107], v[28:29], v[70:71]
	v_pk_add_f32 v[74:75], v[74:75], v[106:107]
	v_pk_fma_f32 v[78:79], v[106:107], v[20:21], v[78:79]
	v_pk_add_f32 v[66:67], v[66:67], v[108:109]
	v_pk_fma_f32 v[70:71], v[108:109], v[30:31], v[70:71]
	v_pk_add_f32 v[74:75], v[74:75], v[110:111]
	v_pk_fma_f32 v[78:79], v[110:111], v[22:23], v[78:79]
	v_pk_add_f32 v[104:105], v[30:31], v[28:29] neg_lo:[0,1] neg_hi:[0,1]
	v_pk_fma_f32 v[104:105], v[104:105], v[104:105], s[22:23] neg_lo:[1,0,0] neg_hi:[1,0,0]
	s_nop 0
	v_exp_f32_e32 v104, v104
	v_exp_f32_e32 v105, v105
	s_nop 0
	v_pk_add_f32 v[64:65], v[64:65], v[96:97]
	v_pk_fma_f32 v[68:69], v[96:97], v[26:27], v[68:69] op_sel:[0,1,0] op_sel_hi:[1,0,1]
	v_pk_add_f32 v[72:73], v[72:73], v[96:97] op_sel:[0,1] op_sel_hi:[1,0]
	v_pk_fma_f32 v[76:77], v[96:97], v[18:19], v[76:77] op_sel:[1,1,0] op_sel_hi:[0,0,1]
	v_pk_add_f32 v[66:67], v[66:67], v[98:99]
	v_pk_fma_f32 v[70:71], v[98:99], v[28:29], v[70:71] op_sel:[0,1,0] op_sel_hi:[1,0,1]
	v_pk_add_f32 v[74:75], v[74:75], v[98:99] op_sel:[0,1] op_sel_hi:[1,0]
	v_pk_fma_f32 v[78:79], v[98:99], v[20:21], v[78:79] op_sel:[1,1,0] op_sel_hi:[0,0,1]
	v_pk_add_f32 v[72:73], v[72:73], v[100:101]
	v_pk_fma_f32 v[76:77], v[100:101], v[24:25], v[76:77]
	v_pk_add_f32 v[74:75], v[74:75], v[102:103]
	v_pk_add_f32 v[72:73], v[72:73], v[102:103]
	v_pk_fma_f32 v[76:77], v[102:103], v[28:29], v[76:77]
	v_pk_fma_f32 v[78:79], v[102:103], v[26:27], v[78:79]
	s_nop 0
	v_sub_f32_e32 v96, v26, v9
	v_sub_f32_e32 v98, v28, v11
	v_sub_f32_e32 v100, v27, v12
	v_sub_f32_e32 v102, v29, v14
	v_sub_f32_e32 v97, v26, v17
	v_sub_f32_e32 v99, v25, v18
	v_sub_f32_e32 v101, v28, v19
	v_sub_f32_e32 v103, v27, v20
	s_nop 0
	v_fma_f32 v96, -v96, v96, s26
	v_fma_f32 v98, -v98, v98, s26
	v_fma_f32 v100, -v100, v100, s26
	v_fma_f32 v102, -v102, v102, s26
	v_fma_f32 v97, -v97, v97, s24
	v_fma_f32 v99, -v99, v99, s24
	v_fma_f32 v101, -v101, v101, s24
	v_fma_f32 v103, -v103, v103, s24
	v_exp_f32_e32 v96, v96
	v_exp_f32_e32 v98, v98
	v_exp_f32_e32 v100, v100
	v_exp_f32_e32 v102, v102
	v_exp_f32_e32 v97, v97
	v_exp_f32_e32 v99, v99
	v_exp_f32_e32 v101, v101
	v_exp_f32_e32 v103, v103
	v_pk_add_f32 v[74:75], v[74:75], v[104:105]
	v_pk_fma_f32 v[78:79], v[104:105], v[30:31], v[78:79]
	v_sub_f32_e32 v108, v30, v21
	v_sub_f32_e32 v110, v29, v22
	v_sub_f32_e32 v105, v26, v25
	v_sub_f32_e32 v104, v27, v26
	v_sub_f32_e32 v107, v28, v27
	v_sub_f32_e32 v106, v29, v28
	v_sub_f32_e32 v109, v30, v29
	s_nop 0
	v_fma_f32 v108, -v108, v108, s24
	v_fma_f32 v110, -v110, v110, s24
	v_fma_f32 v105, -v105, v105, s20
	v_fma_f32 v104, -v104, v104, s20
	v_fma_f32 v107, -v107, v107, s20
	v_fma_f32 v106, -v106, v106, s20
	v_fma_f32 v109, -v109, v109, s20
	v_exp_f32_e32 v108, v108
	v_exp_f32_e32 v110, v110
	v_exp_f32_e32 v105, v105
	v_exp_f32_e32 v104, v104
	v_exp_f32_e32 v107, v107
	v_exp_f32_e32 v106, v106
	v_exp_f32_e32 v109, v109
	v_add_f32_e32 v72, v72, v96
	v_fmac_f32_e32 v76, v96, v9
	v_add_f32_e32 v74, v74, v98
	v_fmac_f32_e32 v78, v98, v11
	v_add_f32_e32 v73, v73, v100
	v_fmac_f32_e32 v77, v100, v12
	v_add_f32_e32 v75, v75, v102
	v_fmac_f32_e32 v79, v102, v14
	v_add_f32_e32 v72, v72, v97
	v_fmac_f32_e32 v76, v97, v17
	v_add_f32_e32 v64, v64, v99
	v_fmac_f32_e32 v68, v99, v25
	v_add_f32_e32 v65, v65, v101
	v_fmac_f32_e32 v69, v101, v28
	v_add_f32_e32 v74, v74, v101
	v_fmac_f32_e32 v78, v101, v19
	v_add_f32_e32 v66, v66, v103
	v_fmac_f32_e32 v70, v103, v27
	v_add_f32_e32 v73, v73, v103
	v_fmac_f32_e32 v77, v103, v20
	v_add_f32_e32 v67, v67, v108
	v_fmac_f32_e32 v71, v108, v30
	v_add_f32_e32 v75, v75, v110
	v_fmac_f32_e32 v79, v110, v22
	v_add_f32_e32 v72, v72, v105
	v_fmac_f32_e32 v76, v105, v25
	v_add_f32_e32 v73, v73, v107
	v_fmac_f32_e32 v77, v107, v28
	v_add_f32_e32 v74, v74, v107
	v_fmac_f32_e32 v78, v107, v27
	v_add_f32_e32 v75, v75, v109
	v_fmac_f32_e32 v79, v109, v30
	s_nop 0
	v_pk_add_f32 v[72:73], v[72:73], v[104:105] op_sel_hi:[1,0]
	v_pk_fma_f32 v[76:77], v[104:105], v[26:27], v[76:77] op_sel:[0,1,0] op_sel_hi:[0,0,1]
	v_pk_add_f32 v[74:75], v[74:75], v[106:107] op_sel_hi:[1,0]
	v_pk_fma_f32 v[78:79], v[106:107], v[28:29], v[78:79] op_sel:[0,1,0] op_sel_hi:[0,0,1]
	s_waitcnt vmcnt(9)
	s_nop 0
	v_mov_b32_dpp v32, v36 row_shr:1 row_mask:0xf bank_mask:0xf
	v_mov_b32_dpp v33, v37 row_shr:1 row_mask:0xf bank_mask:0xf
	v_mov_b32_dpp v38, v34 row_shl:1 row_mask:0xf bank_mask:0xf
	v_mov_b32_dpp v39, v35 row_shl:1 row_mask:0xf bank_mask:0xf
	v_pk_mul_f32 v[34:35], v[34:35], s[32:33]
	v_pk_mul_f32 v[36:37], v[36:37], s[32:33]
	v_cndmask_b32_e64 v33, v33, v32, vcc
	v_cndmask_b32_e64 v38, v38, v39, s[16:17]
	v_pk_mul_f32 v[84:85], v[34:35], s[30:31]
	v_pk_mul_f32 v[86:87], v[36:37], s[30:31]
	v_pk_mul_f32 v[32:33], v[32:33], s[32:33]
	v_pk_mul_f32 v[38:39], v[38:39], s[32:33]
	v_mov_b32_e32 v80, s30
	v_mov_b32_e32 v81, s30
	v_mov_b32_e32 v82, s30
	v_mov_b32_e32 v83, s30
	s_setprio 2
	s_nop 0
	v_pk_add_f32 v[96:97], v[34:35], v[16:17] neg_lo:[0,1] neg_hi:[0,1]
	v_pk_add_f32 v[98:99], v[32:33], v[18:19] neg_lo:[0,1] neg_hi:[0,1]
	v_pk_add_f32 v[100:101], v[34:35], v[18:19] neg_lo:[0,1] neg_hi:[0,1]
	v_pk_add_f32 v[102:103], v[36:37], v[18:19] neg_lo:[0,1] neg_hi:[0,1]
	v_pk_fma_f32 v[96:97], v[96:97], v[96:97], s[28:29] neg_lo:[1,0,0] neg_hi:[1,0,0]
	v_pk_fma_f32 v[98:99], v[98:99], v[98:99], s[28:29] neg_lo:[1,0,0] neg_hi:[1,0,0]
	v_pk_fma_f32 v[100:101], v[100:101], v[100:101], s[22:23] neg_lo:[1,0,0] neg_hi:[1,0,0]
	v_pk_fma_f32 v[102:103], v[102:103], v[102:103], s[28:29] neg_lo:[1,0,0] neg_hi:[1,0,0]
	v_exp_f32_e32 v96, v96
	v_exp_f32_e32 v97, v97
	v_exp_f32_e32 v98, v98
	v_exp_f32_e32 v99, v99
	v_exp_f32_e32 v100, v100
	v_exp_f32_e32 v101, v101
	v_exp_f32_e32 v102, v102
	v_exp_f32_e32 v103, v103
	v_pk_add_f32 v[104:105], v[34:35], v[20:21] neg_lo:[0,1] neg_hi:[0,1]
	v_pk_add_f32 v[106:107], v[36:37], v[20:21] neg_lo:[0,1] neg_hi:[0,1]
	v_pk_add_f32 v[108:109], v[38:39], v[20:21] neg_lo:[0,1] neg_hi:[0,1]
	v_pk_add_f32 v[110:111], v[36:37], v[22:23] neg_lo:[0,1] neg_hi:[0,1]
	v_pk_fma_f32 v[104:105], v[104:105], v[104:105], s[28:29] neg_lo:[1,0,0] neg_hi:[1,0,0]
	v_pk_fma_f32 v[106:107], v[106:107], v[106:107], s[22:23] neg_lo:[1,0,0] neg_hi:[1,0,0]
	v_pk_fma_f32 v[108:109], v[108:109], v[108:109], s[28:29] neg_lo:[1,0,0] neg_hi:[1,0,0]
	v_pk_fma_f32 v[110:111], v[110:111], v[110:111], s[28:29] neg_lo:[1,0,0] neg_hi:[1,0,0]
	v_exp_f32_e32 v104, v104
	v_exp_f32_e32 v105, v105
	v_exp_f32_e32 v106, v106
	v_exp_f32_e32 v107, v107
	v_exp_f32_e32 v108, v108
	v_exp_f32_e32 v109, v109
	v_exp_f32_e32 v110, v110
	v_exp_f32_e32 v111, v111
	v_pk_add_f32 v[80:81], v[80:81], v[96:97]
	v_pk_fma_f32 v[84:85], v[96:97], v[16:17], v[84:85]
	v_pk_add_f32 v[64:65], v[64:65], v[98:99]
	v_pk_fma_f32 v[68:69], v[98:99], v[32:33], v[68:69]
	v_pk_add_f32 v[80:81], v[80:81], v[100:101]
	v_pk_add_f32 v[64:65], v[64:65], v[100:101]
	v_pk_fma_f32 v[68:69], v[100:101], v[34:35], v[68:69]
	v_pk_fma_f32 v[84:85], v[100:101], v[18:19], v[84:85]
	v_pk_add_f32 v[64:65], v[64:65], v[102:103]
	v_pk_fma_f32 v[68:69], v[102:103], v[36:37], v[68:69]
	v_pk_add_f32 v[82:83], v[82:83], v[102:103]
	v_pk_fma_f32 v[86:87], v[102:103], v[18:19], v[86:87]
	v_pk_add_f32 v[96:97], v[34:35], v[18:19] op_sel:[1,0] op_sel_hi:[0,1] neg_lo:[0,1] neg_hi:[0,1]
	v_pk_add_f32 v[98:99], v[36:37], v[20:21] op_sel:[1,0] op_sel_hi:[0,1] neg_lo:[0,1] neg_hi:[0,1]
	v_pk_add_f32 v[100:101], v[34:35], v[24:25] neg_lo:[0,1] neg_hi:[0,1]
	v_pk_add_f32 v[102:103], v[32:33], v[26:27] neg_lo:[0,1] neg_hi:[0,1]
	v_pk_fma_f32 v[96:97], v[96:97], v[96:97], s[26:27] neg_lo:[1,0,0] neg_hi:[1,0,0]
	v_pk_fma_f32 v[98:99], v[98:99], v[98:99], s[26:27] neg_lo:[1,0,0] neg_hi:[1,0,0]
	v_pk_fma_f32 v[100:101], v[100:101], v[100:101], s[26:27] neg_lo:[1,0,0] neg_hi:[1,0,0]
	v_pk_fma_f32 v[102:103], v[102:103], v[102:103], s[26:27] neg_lo:[1,0,0] neg_hi:[1,0,0]
	v_exp_f32_e32 v96, v96
	v_exp_f32_e32 v97, v97
	v_exp_f32_e32 v98, v98
	v_exp_f32_e32 v99, v99
	v_exp_f32_e32 v100, v100
	v_exp_f32_e32 v101, v101
	v_exp_f32_e32 v102, v102
	v_exp_f32_e32 v103, v103
	v_pk_add_f32 v[66:67], v[66:67], v[104:105]
	v_pk_fma_f32 v[70:71], v[104:105], v[34:35], v[70:71]
	v_pk_add_f32 v[80:81], v[80:81], v[104:105]
	v_pk_fma_f32 v[84:85], v[104:105], v[20:21], v[84:85]
	v_pk_add_f32 v[66:67], v[66:67], v[106:107]
	v_pk_fma_f32 v[70:71], v[106:107], v[36:37], v[70:71]
	v_pk_add_f32 v[82:83], v[82:83], v[106:107]
	v_pk_fma_f32 v[86:87], v[106:107], v[20:21], v[86:87]
	v_pk_add_f32 v[66:67], v[66:67], v[108:109]
	v_pk_fma_f32 v[70:71], v[108:109], v[38:39], v[70:71]
	v_pk_add_f32 v[82:83], v[82:83], v[110:111]
	v_pk_fma_f32 v[86:87], v[110:111], v[22:23], v[86:87]
	v_pk_add_f32 v[104:105], v[34:35], v[26:27] neg_lo:[0,1] neg_hi:[0,1]
	v_pk_add_f32 v[106:107], v[36:37], v[26:27] neg_lo:[0,1] neg_hi:[0,1]
	v_pk_add_f32 v[108:109], v[34:35], v[28:29] neg_lo:[0,1] neg_hi:[0,1]
	v_pk_add_f32 v[110:111], v[36:37], v[28:29] neg_lo:[0,1] neg_hi:[0,1]
	v_pk_fma_f32 v[104:105], v[104:105], v[104:105], s[20:21] neg_lo:[1,0,0] neg_hi:[1,0,0]
	v_pk_fma_f32 v[106:107], v[106:107], v[106:107], s[26:27] neg_lo:[1,0,0] neg_hi:[1,0,0]
	v_pk_fma_f32 v[108:109], v[108:109], v[108:109], s[26:27] neg_lo:[1,0,0] neg_hi:[1,0,0]
	v_pk_fma_f32 v[110:111], v[110:111], v[110:111], s[20:21] neg_lo:[1,0,0] neg_hi:[1,0,0]
	v_exp_f32_e32 v104, v104
	v_exp_f32_e32 v105, v105
	v_exp_f32_e32 v106, v106
	v_exp_f32_e32 v107, v107
	v_exp_f32_e32 v108, v108
	v_exp_f32_e32 v109, v109
	v_exp_f32_e32 v110, v110
	v_exp_f32_e32 v111, v111
	v_pk_add_f32 v[64:65], v[64:65], v[96:97]
	v_pk_fma_f32 v[68:69], v[96:97], v[34:35], v[68:69] op_sel:[0,1,0] op_sel_hi:[1,0,1]
	v_pk_add_f32 v[80:81], v[80:81], v[96:97] op_sel:[0,1] op_sel_hi:[1,0]
	v_pk_fma_f32 v[84:85], v[96:97], v[18:19], v[84:85] op_sel:[1,1,0] op_sel_hi:[0,0,1]
	v_pk_add_f32 v[66:67], v[66:67], v[98:99]
	v_pk_fma_f32 v[70:71], v[98:99], v[36:37], v[70:71] op_sel:[0,1,0] op_sel_hi:[1,0,1]
	v_pk_add_f32 v[82:83], v[82:83], v[98:99] op_sel:[0,1] op_sel_hi:[1,0]
	v_pk_fma_f32 v[86:87], v[98:99], v[20:21], v[86:87] op_sel:[1,1,0] op_sel_hi:[0,0,1]
	v_pk_add_f32 v[80:81], v[80:81], v[100:101]
	v_pk_fma_f32 v[84:85], v[100:101], v[24:25], v[84:85]
	v_pk_add_f32 v[72:73], v[72:73], v[102:103]
	v_pk_fma_f32 v[76:77], v[102:103], v[32:33], v[76:77]
	v_pk_add_f32 v[96:97], v[38:39], v[28:29] neg_lo:[0,1] neg_hi:[0,1]
	v_pk_add_f32 v[98:99], v[36:37], v[30:31] neg_lo:[0,1] neg_hi:[0,1]
	v_pk_add_f32 v[100:101], v[34:35], v[26:27] op_sel:[1,0] op_sel_hi:[0,1] neg_lo:[0,1] neg_hi:[0,1]
	v_pk_add_f32 v[102:103], v[36:37], v[28:29] op_sel:[1,0] op_sel_hi:[0,1] neg_lo:[0,1] neg_hi:[0,1]
	v_pk_fma_f32 v[96:97], v[96:97], v[96:97], s[26:27] neg_lo:[1,0,0] neg_hi:[1,0,0]
	v_pk_fma_f32 v[98:99], v[98:99], v[98:99], s[26:27] neg_lo:[1,0,0] neg_hi:[1,0,0]
	v_pk_fma_f32 v[100:101], v[100:101], v[100:101], s[24:25] neg_lo:[1,0,0] neg_hi:[1,0,0]
	v_pk_fma_f32 v[102:103], v[102:103], v[102:103], s[24:25] neg_lo:[1,0,0] neg_hi:[1,0,0]
	v_exp_f32_e32 v96, v96
	v_exp_f32_e32 v97, v97
	v_exp_f32_e32 v98, v98
	v_exp_f32_e32 v99, v99
	v_exp_f32_e32 v100, v100
	v_exp_f32_e32 v101, v101
	v_exp_f32_e32 v102, v102
	v_exp_f32_e32 v103, v103
	v_pk_add_f32 v[72:73], v[72:73], v[104:105]
	v_pk_fma_f32 v[76:77], v[104:105], v[34:35], v[76:77]
	v_pk_add_f32 v[80:81], v[80:81], v[104:105]
	v_pk_fma_f32 v[84:85], v[104:105], v[26:27], v[84:85]
	v_pk_add_f32 v[72:73], v[72:73], v[106:107]
	v_pk_fma_f32 v[76:77], v[106:107], v[36:37], v[76:77]
	v_pk_add_f32 v[82:83], v[82:83], v[106:107]
	v_pk_fma_f32 v[86:87], v[106:107], v[26:27], v[86:87]
	v_pk_add_f32 v[74:75], v[74:75], v[108:109]
	v_pk_fma_f32 v[78:79], v[108:109], v[34:35], v[78:79]
	v_pk_add_f32 v[80:81], v[80:81], v[108:109]
	v_pk_fma_f32 v[84:85], v[108:109], v[28:29], v[84:85]
	v_pk_add_f32 v[74:75], v[74:75], v[110:111]
	v_pk_fma_f32 v[78:79], v[110:111], v[36:37], v[78:79]
	v_pk_add_f32 v[82:83], v[82:83], v[110:111]
	v_pk_fma_f32 v[86:87], v[110:111], v[28:29], v[86:87]
	v_pk_add_f32 v[104:105], v[34:35], v[32:33] neg_lo:[0,1] neg_hi:[0,1]
	v_pk_add_f32 v[106:107], v[36:37], v[34:35] neg_lo:[0,1] neg_hi:[0,1]
	v_pk_add_f32 v[108:109], v[38:39], v[36:37] neg_lo:[0,1] neg_hi:[0,1]
	v_pk_fma_f32 v[104:105], v[104:105], v[104:105], s[22:23] neg_lo:[1,0,0] neg_hi:[1,0,0]
	v_pk_fma_f32 v[106:107], v[106:107], v[106:107], s[22:23] neg_lo:[1,0,0] neg_hi:[1,0,0]
	v_pk_fma_f32 v[108:109], v[108:109], v[108:109], s[22:23] neg_lo:[1,0,0] neg_hi:[1,0,0]
	v_exp_f32_e32 v104, v104
	v_exp_f32_e32 v105, v105
	v_exp_f32_e32 v106, v106
	v_exp_f32_e32 v107, v107
	v_exp_f32_e32 v108, v108
	v_exp_f32_e32 v109, v109
	v_pk_add_f32 v[74:75], v[74:75], v[96:97]
	v_pk_fma_f32 v[78:79], v[96:97], v[38:39], v[78:79]
	v_pk_add_f32 v[82:83], v[82:83], v[98:99]
	v_pk_fma_f32 v[86:87], v[98:99], v[30:31], v[86:87]
	v_pk_add_f32 v[72:73], v[72:73], v[100:101]
	v_pk_fma_f32 v[76:77], v[100:101], v[34:35], v[76:77] op_sel:[0,1,0] op_sel_hi:[1,0,1]
	v_pk_add_f32 v[80:81], v[80:81], v[100:101] op_sel:[0,1] op_sel_hi:[1,0]
	v_pk_fma_f32 v[84:85], v[100:101], v[26:27], v[84:85] op_sel:[1,1,0] op_sel_hi:[0,0,1]
	v_pk_add_f32 v[74:75], v[74:75], v[102:103]
	v_pk_fma_f32 v[78:79], v[102:103], v[36:37], v[78:79] op_sel:[0,1,0] op_sel_hi:[1,0,1]
	v_pk_add_f32 v[82:83], v[82:83], v[102:103] op_sel:[0,1] op_sel_hi:[1,0]
	v_pk_fma_f32 v[86:87], v[102:103], v[28:29], v[86:87] op_sel:[1,1,0] op_sel_hi:[0,0,1]
	v_sub_f32_e32 v96, v34, v17
	v_sub_f32_e32 v98, v33, v18
	v_sub_f32_e32 v100, v36, v19
	v_sub_f32_e32 v102, v35, v20
	v_sub_f32_e32 v97, v38, v21
	v_sub_f32_e32 v99, v37, v22
	v_sub_f32_e32 v101, v34, v25
	v_sub_f32_e32 v103, v33, v26
	v_fma_f32 v96, -v96, v96, s26
	v_fma_f32 v98, -v98, v98, s26
	v_fma_f32 v100, -v100, v100, s26
	v_fma_f32 v102, -v102, v102, s26
	v_fma_f32 v97, -v97, v97, s26
	v_fma_f32 v99, -v99, v99, s26
	v_fma_f32 v101, -v101, v101, s24
	v_fma_f32 v103, -v103, v103, s24
	v_exp_f32_e32 v96, v96
	v_exp_f32_e32 v98, v98
	v_exp_f32_e32 v100, v100
	v_exp_f32_e32 v102, v102
	v_exp_f32_e32 v97, v97
	v_exp_f32_e32 v99, v99
	v_exp_f32_e32 v101, v101
	v_exp_f32_e32 v103, v103
	v_pk_add_f32 v[80:81], v[80:81], v[104:105]
	v_pk_fma_f32 v[84:85], v[104:105], v[32:33], v[84:85]
	v_pk_add_f32 v[82:83], v[82:83], v[106:107]
	v_pk_add_f32 v[80:81], v[80:81], v[106:107]
	v_pk_fma_f32 v[84:85], v[106:107], v[36:37], v[84:85]
	v_pk_fma_f32 v[86:87], v[106:107], v[34:35], v[86:87]
	v_pk_add_f32 v[82:83], v[82:83], v[108:109]
	v_pk_fma_f32 v[86:87], v[108:109], v[38:39], v[86:87]
	v_sub_f32_e32 v108, v36, v27
	v_sub_f32_e32 v110, v35, v28
	v_sub_f32_e32 v105, v38, v29
	v_sub_f32_e32 v107, v37, v30
	v_sub_f32_e32 v109, v34, v33
	v_sub_f32_e32 v104, v35, v34
	v_sub_f32_e32 v111, v36, v35
	v_sub_f32_e32 v106, v37, v36
	v_fma_f32 v108, -v108, v108, s24
	v_fma_f32 v110, -v110, v110, s24
	v_fma_f32 v105, -v105, v105, s24
	v_fma_f32 v107, -v107, v107, s24
	v_fma_f32 v109, -v109, v109, s20
	v_fma_f32 v104, -v104, v104, s20
	v_fma_f32 v111, -v111, v111, s20
	v_fma_f32 v106, -v106, v106, s20
	v_exp_f32_e32 v108, v108
	v_exp_f32_e32 v110, v110
	v_exp_f32_e32 v105, v105
	v_exp_f32_e32 v107, v107
	v_exp_f32_e32 v109, v109
	v_exp_f32_e32 v104, v104
	v_exp_f32_e32 v111, v111
	v_exp_f32_e32 v106, v106
	v_add_f32_e32 v80, v80, v96
	v_fmac_f32_e32 v84, v96, v17
	v_add_f32_e32 v64, v64, v98
	v_fmac_f32_e32 v68, v98, v33
	v_add_f32_e32 v65, v65, v100
	v_fmac_f32_e32 v69, v100, v36
	v_add_f32_e32 v82, v82, v100
	v_fmac_f32_e32 v86, v100, v19
	v_add_f32_e32 v66, v66, v102
	v_fmac_f32_e32 v70, v102, v35
	v_add_f32_e32 v81, v81, v102
	v_fmac_f32_e32 v85, v102, v20
	v_add_f32_e32 v67, v67, v97
	v_fmac_f32_e32 v71, v97, v38
	v_add_f32_e32 v83, v83, v99
	v_fmac_f32_e32 v87, v99, v22
	v_add_f32_e32 v80, v80, v101
	v_fmac_f32_e32 v84, v101, v25
	v_add_f32_e32 v72, v72, v103
	v_fmac_f32_e32 v76, v103, v33
	v_sub_f32_e32 v96, v38, v37
	s_nop 0
	v_fma_f32 v96, -v96, v96, s20
	s_nop 0
	v_exp_f32_e32 v96, v96
	v_add_f32_e32 v73, v73, v108
	v_fmac_f32_e32 v77, v108, v36
	v_add_f32_e32 v82, v82, v108
	v_fmac_f32_e32 v86, v108, v27
	v_add_f32_e32 v74, v74, v110
	v_fmac_f32_e32 v78, v110, v35
	v_add_f32_e32 v81, v81, v110
	v_fmac_f32_e32 v85, v110, v28
	v_add_f32_e32 v75, v75, v105
	v_fmac_f32_e32 v79, v105, v38
	v_add_f32_e32 v83, v83, v107
	v_fmac_f32_e32 v87, v107, v30
	v_add_f32_e32 v80, v80, v109
	v_fmac_f32_e32 v84, v109, v33
	v_add_f32_e32 v81, v81, v111
	v_fmac_f32_e32 v85, v111, v36
	v_add_f32_e32 v82, v82, v111
	v_fmac_f32_e32 v86, v111, v35
	v_pk_add_f32 v[80:81], v[80:81], v[104:105] op_sel_hi:[1,0]
	v_pk_fma_f32 v[84:85], v[104:105], v[34:35], v[84:85] op_sel:[0,1,0] op_sel_hi:[0,0,1]
	v_pk_add_f32 v[82:83], v[82:83], v[106:107] op_sel_hi:[1,0]
	v_pk_fma_f32 v[86:87], v[106:107], v[36:37], v[86:87] op_sel:[0,1,0] op_sel_hi:[0,0,1]
	s_nop 0
	v_add_f32_e32 v83, v83, v96
	v_fmac_f32_e32 v87, v96, v38
	v_rcp_f32_e32 v96, v64
	v_rcp_f32_e32 v97, v65
	v_rcp_f32_e32 v98, v66
	v_rcp_f32_e32 v99, v67
	s_nop 0
	v_pk_mul_f32 v[68:69], v[68:69], s[34:35]
	v_pk_mul_f32 v[70:71], v[70:71], s[34:35]
	v_pk_mul_f32 v[68:69], v[68:69], v[96:97]
	v_pk_mul_f32 v[70:71], v[70:71], v[98:99]
	s_nop 0
	s_nop 0
	buffer_store_dwordx4 v[68:71], v114, s[12:15], 0 offen sc1
	s_waitcnt vmcnt(7)
	s_nop 0
	v_mov_b32_dpp v40, v44 row_shr:1 row_mask:0xf bank_mask:0xf
	v_mov_b32_dpp v41, v45 row_shr:1 row_mask:0xf bank_mask:0xf
	v_mov_b32_dpp v46, v42 row_shl:1 row_mask:0xf bank_mask:0xf
	v_mov_b32_dpp v47, v43 row_shl:1 row_mask:0xf bank_mask:0xf
	v_pk_mul_f32 v[42:43], v[42:43], s[32:33]
	v_pk_mul_f32 v[44:45], v[44:45], s[32:33]
	v_cndmask_b32_e64 v41, v41, v40, vcc
	v_cndmask_b32_e64 v46, v46, v47, s[16:17]
	v_pk_mul_f32 v[92:93], v[42:43], s[30:31]
	v_pk_mul_f32 v[94:95], v[44:45], s[30:31]
	v_pk_mul_f32 v[40:41], v[40:41], s[32:33]
	v_pk_mul_f32 v[46:47], v[46:47], s[32:33]
	v_mov_b32_e32 v88, s30
	v_mov_b32_e32 v89, s30
	v_mov_b32_e32 v90, s30
	v_mov_b32_e32 v91, s30
	s_setprio 1
	s_nop 0
	v_pk_add_f32 v[96:97], v[42:43], v[24:25] neg_lo:[0,1] neg_hi:[0,1]
	v_pk_add_f32 v[98:99], v[40:41], v[26:27] neg_lo:[0,1] neg_hi:[0,1]
	v_pk_add_f32 v[100:101], v[42:43], v[26:27] neg_lo:[0,1] neg_hi:[0,1]
	v_pk_add_f32 v[102:103], v[44:45], v[26:27] neg_lo:[0,1] neg_hi:[0,1]
	v_pk_fma_f32 v[96:97], v[96:97], v[96:97], s[28:29] neg_lo:[1,0,0] neg_hi:[1,0,0]
	v_pk_fma_f32 v[98:99], v[98:99], v[98:99], s[28:29] neg_lo:[1,0,0] neg_hi:[1,0,0]
	v_pk_fma_f32 v[100:101], v[100:101], v[100:101], s[22:23] neg_lo:[1,0,0] neg_hi:[1,0,0]
	v_pk_fma_f32 v[102:103], v[102:103], v[102:103], s[28:29] neg_lo:[1,0,0] neg_hi:[1,0,0]
	v_exp_f32_e32 v96, v96
	v_exp_f32_e32 v97, v97
	v_exp_f32_e32 v98, v98
	v_exp_f32_e32 v99, v99
	v_exp_f32_e32 v100, v100
	v_exp_f32_e32 v101, v101
	v_exp_f32_e32 v102, v102
	v_exp_f32_e32 v103, v103
	v_pk_add_f32 v[104:105], v[42:43], v[28:29] neg_lo:[0,1] neg_hi:[0,1]
	v_pk_add_f32 v[106:107], v[44:45], v[28:29] neg_lo:[0,1] neg_hi:[0,1]
	v_pk_add_f32 v[108:109], v[46:47], v[28:29] neg_lo:[0,1] neg_hi:[0,1]
	v_pk_add_f32 v[110:111], v[44:45], v[30:31] neg_lo:[0,1] neg_hi:[0,1]
	v_pk_fma_f32 v[104:105], v[104:105], v[104:105], s[28:29] neg_lo:[1,0,0] neg_hi:[1,0,0]
	v_pk_fma_f32 v[106:107], v[106:107], v[106:107], s[22:23] neg_lo:[1,0,0] neg_hi:[1,0,0]
	v_pk_fma_f32 v[108:109], v[108:109], v[108:109], s[28:29] neg_lo:[1,0,0] neg_hi:[1,0,0]
	v_pk_fma_f32 v[110:111], v[110:111], v[110:111], s[28:29] neg_lo:[1,0,0] neg_hi:[1,0,0]
	v_exp_f32_e32 v104, v104
	v_exp_f32_e32 v105, v105
	v_exp_f32_e32 v106, v106
	v_exp_f32_e32 v107, v107
	v_exp_f32_e32 v108, v108
	v_exp_f32_e32 v109, v109
	v_exp_f32_e32 v110, v110
	v_exp_f32_e32 v111, v111
	v_pk_add_f32 v[88:89], v[88:89], v[96:97]
	v_pk_fma_f32 v[92:93], v[96:97], v[24:25], v[92:93]
	v_pk_add_f32 v[72:73], v[72:73], v[98:99]
	v_pk_fma_f32 v[76:77], v[98:99], v[40:41], v[76:77]
	v_pk_add_f32 v[88:89], v[88:89], v[100:101]
	v_pk_add_f32 v[72:73], v[72:73], v[100:101]
	v_pk_fma_f32 v[76:77], v[100:101], v[42:43], v[76:77]
	v_pk_fma_f32 v[92:93], v[100:101], v[26:27], v[92:93]
	v_pk_add_f32 v[72:73], v[72:73], v[102:103]
	v_pk_fma_f32 v[76:77], v[102:103], v[44:45], v[76:77]
	v_pk_add_f32 v[90:91], v[90:91], v[102:103]
	v_pk_fma_f32 v[94:95], v[102:103], v[26:27], v[94:95]
	v_pk_add_f32 v[96:97], v[42:43], v[26:27] op_sel:[1,0] op_sel_hi:[0,1] neg_lo:[0,1] neg_hi:[0,1]
	v_pk_add_f32 v[98:99], v[44:45], v[28:29] op_sel:[1,0] op_sel_hi:[0,1] neg_lo:[0,1] neg_hi:[0,1]
	v_pk_add_f32 v[100:101], v[42:43], v[32:33] neg_lo:[0,1] neg_hi:[0,1]
	v_pk_add_f32 v[102:103], v[40:41], v[34:35] neg_lo:[0,1] neg_hi:[0,1]
	v_pk_fma_f32 v[96:97], v[96:97], v[96:97], s[26:27] neg_lo:[1,0,0] neg_hi:[1,0,0]
	v_pk_fma_f32 v[98:99], v[98:99], v[98:99], s[26:27] neg_lo:[1,0,0] neg_hi:[1,0,0]
	v_pk_fma_f32 v[100:101], v[100:101], v[100:101], s[26:27] neg_lo:[1,0,0] neg_hi:[1,0,0]
	v_pk_fma_f32 v[102:103], v[102:103], v[102:103], s[26:27] neg_lo:[1,0,0] neg_hi:[1,0,0]
	v_exp_f32_e32 v96, v96
	v_exp_f32_e32 v97, v97
	v_exp_f32_e32 v98, v98
	v_exp_f32_e32 v99, v99
	v_exp_f32_e32 v100, v100
	v_exp_f32_e32 v101, v101
	v_exp_f32_e32 v102, v102
	v_exp_f32_e32 v103, v103
	v_pk_add_f32 v[74:75], v[74:75], v[104:105]
	v_pk_fma_f32 v[78:79], v[104:105], v[42:43], v[78:79]
	v_pk_add_f32 v[88:89], v[88:89], v[104:105]
	v_pk_fma_f32 v[92:93], v[104:105], v[28:29], v[92:93]
	v_pk_add_f32 v[74:75], v[74:75], v[106:107]
	v_pk_fma_f32 v[78:79], v[106:107], v[44:45], v[78:79]
	v_pk_add_f32 v[90:91], v[90:91], v[106:107]
	v_pk_fma_f32 v[94:95], v[106:107], v[28:29], v[94:95]
	v_pk_add_f32 v[74:75], v[74:75], v[108:109]
	v_pk_fma_f32 v[78:79], v[108:109], v[46:47], v[78:79]
	v_pk_add_f32 v[90:91], v[90:91], v[110:111]
	v_pk_fma_f32 v[94:95], v[110:111], v[30:31], v[94:95]
	v_pk_add_f32 v[104:105], v[42:43], v[34:35] neg_lo:[0,1] neg_hi:[0,1]
	v_pk_add_f32 v[106:107], v[44:45], v[34:35] neg_lo:[0,1] neg_hi:[0,1]
	v_pk_add_f32 v[108:109], v[42:43], v[36:37] neg_lo:[0,1] neg_hi:[0,1]
	v_pk_add_f32 v[110:111], v[44:45], v[36:37] neg_lo:[0,1] neg_hi:[0,1]
	v_pk_fma_f32 v[104:105], v[104:105], v[104:105], s[20:21] neg_lo:[1,0,0] neg_hi:[1,0,0]
	v_pk_fma_f32 v[106:107], v[106:107], v[106:107], s[26:27] neg_lo:[1,0,0] neg_hi:[1,0,0]
	v_pk_fma_f32 v[108:109], v[108:109], v[108:109], s[26:27] neg_lo:[1,0,0] neg_hi:[1,0,0]
	v_pk_fma_f32 v[110:111], v[110:111], v[110:111], s[20:21] neg_lo:[1,0,0] neg_hi:[1,0,0]
	v_exp_f32_e32 v104, v104
	v_exp_f32_e32 v105, v105
	v_exp_f32_e32 v106, v106
	v_exp_f32_e32 v107, v107
	v_exp_f32_e32 v108, v108
	v_exp_f32_e32 v109, v109
	v_exp_f32_e32 v110, v110
	v_exp_f32_e32 v111, v111
	v_pk_add_f32 v[72:73], v[72:73], v[96:97]
	v_pk_fma_f32 v[76:77], v[96:97], v[42:43], v[76:77] op_sel:[0,1,0] op_sel_hi:[1,0,1]
	v_pk_add_f32 v[88:89], v[88:89], v[96:97] op_sel:[0,1] op_sel_hi:[1,0]
	v_pk_fma_f32 v[92:93], v[96:97], v[26:27], v[92:93] op_sel:[1,1,0] op_sel_hi:[0,0,1]
	v_pk_add_f32 v[74:75], v[74:75], v[98:99]
	v_pk_fma_f32 v[78:79], v[98:99], v[44:45], v[78:79] op_sel:[0,1,0] op_sel_hi:[1,0,1]
	v_pk_add_f32 v[90:91], v[90:91], v[98:99] op_sel:[0,1] op_sel_hi:[1,0]
	v_pk_fma_f32 v[94:95], v[98:99], v[28:29], v[94:95] op_sel:[1,1,0] op_sel_hi:[0,0,1]
	v_pk_add_f32 v[88:89], v[88:89], v[100:101]
	v_pk_fma_f32 v[92:93], v[100:101], v[32:33], v[92:93]
	v_pk_add_f32 v[80:81], v[80:81], v[102:103]
	v_pk_fma_f32 v[84:85], v[102:103], v[40:41], v[84:85]
	v_pk_add_f32 v[96:97], v[46:47], v[36:37] neg_lo:[0,1] neg_hi:[0,1]
	v_pk_add_f32 v[98:99], v[44:45], v[38:39] neg_lo:[0,1] neg_hi:[0,1]
	v_pk_add_f32 v[100:101], v[42:43], v[34:35] op_sel:[1,0] op_sel_hi:[0,1] neg_lo:[0,1] neg_hi:[0,1]
	v_pk_add_f32 v[102:103], v[44:45], v[36:37] op_sel:[1,0] op_sel_hi:[0,1] neg_lo:[0,1] neg_hi:[0,1]
	v_pk_fma_f32 v[96:97], v[96:97], v[96:97], s[26:27] neg_lo:[1,0,0] neg_hi:[1,0,0]
	v_pk_fma_f32 v[98:99], v[98:99], v[98:99], s[26:27] neg_lo:[1,0,0] neg_hi:[1,0,0]
	v_pk_fma_f32 v[100:101], v[100:101], v[100:101], s[24:25] neg_lo:[1,0,0] neg_hi:[1,0,0]
	v_pk_fma_f32 v[102:103], v[102:103], v[102:103], s[24:25] neg_lo:[1,0,0] neg_hi:[1,0,0]
	v_exp_f32_e32 v96, v96
	v_exp_f32_e32 v97, v97
	v_exp_f32_e32 v98, v98
	v_exp_f32_e32 v99, v99
	v_exp_f32_e32 v100, v100
	v_exp_f32_e32 v101, v101
	v_exp_f32_e32 v102, v102
	v_exp_f32_e32 v103, v103
	v_pk_add_f32 v[80:81], v[80:81], v[104:105]
	v_pk_fma_f32 v[84:85], v[104:105], v[42:43], v[84:85]
	v_pk_add_f32 v[88:89], v[88:89], v[104:105]
	v_pk_fma_f32 v[92:93], v[104:105], v[34:35], v[92:93]
	v_pk_add_f32 v[80:81], v[80:81], v[106:107]
	v_pk_fma_f32 v[84:85], v[106:107], v[44:45], v[84:85]
	v_pk_add_f32 v[90:91], v[90:91], v[106:107]
	v_pk_fma_f32 v[94:95], v[106:107], v[34:35], v[94:95]
	v_pk_add_f32 v[82:83], v[82:83], v[108:109]
	v_pk_fma_f32 v[86:87], v[108:109], v[42:43], v[86:87]
	v_pk_add_f32 v[88:89], v[88:89], v[108:109]
	v_pk_fma_f32 v[92:93], v[108:109], v[36:37], v[92:93]
	v_pk_add_f32 v[82:83], v[82:83], v[110:111]
	v_pk_fma_f32 v[86:87], v[110:111], v[44:45], v[86:87]
	v_pk_add_f32 v[90:91], v[90:91], v[110:111]
	v_pk_fma_f32 v[94:95], v[110:111], v[36:37], v[94:95]
	v_pk_add_f32 v[104:105], v[42:43], v[40:41] neg_lo:[0,1] neg_hi:[0,1]
	v_pk_add_f32 v[106:107], v[44:45], v[42:43] neg_lo:[0,1] neg_hi:[0,1]
	v_pk_add_f32 v[108:109], v[46:47], v[44:45] neg_lo:[0,1] neg_hi:[0,1]
	v_pk_fma_f32 v[104:105], v[104:105], v[104:105], s[22:23] neg_lo:[1,0,0] neg_hi:[1,0,0]
	v_pk_fma_f32 v[106:107], v[106:107], v[106:107], s[22:23] neg_lo:[1,0,0] neg_hi:[1,0,0]
	v_pk_fma_f32 v[108:109], v[108:109], v[108:109], s[22:23] neg_lo:[1,0,0] neg_hi:[1,0,0]
	v_exp_f32_e32 v104, v104
	v_exp_f32_e32 v105, v105
	v_exp_f32_e32 v106, v106
	v_exp_f32_e32 v107, v107
	v_exp_f32_e32 v108, v108
	v_exp_f32_e32 v109, v109
	v_pk_add_f32 v[82:83], v[82:83], v[96:97]
	v_pk_fma_f32 v[86:87], v[96:97], v[46:47], v[86:87]
	v_pk_add_f32 v[90:91], v[90:91], v[98:99]
	v_pk_fma_f32 v[94:95], v[98:99], v[38:39], v[94:95]
	v_pk_add_f32 v[80:81], v[80:81], v[100:101]
	v_pk_fma_f32 v[84:85], v[100:101], v[42:43], v[84:85] op_sel:[0,1,0] op_sel_hi:[1,0,1]
	v_pk_add_f32 v[88:89], v[88:89], v[100:101] op_sel:[0,1] op_sel_hi:[1,0]
	v_pk_fma_f32 v[92:93], v[100:101], v[34:35], v[92:93] op_sel:[1,1,0] op_sel_hi:[0,0,1]
	v_pk_add_f32 v[82:83], v[82:83], v[102:103]
	v_pk_fma_f32 v[86:87], v[102:103], v[44:45], v[86:87] op_sel:[0,1,0] op_sel_hi:[1,0,1]
	v_pk_add_f32 v[90:91], v[90:91], v[102:103] op_sel:[0,1] op_sel_hi:[1,0]
	v_pk_fma_f32 v[94:95], v[102:103], v[36:37], v[94:95] op_sel:[1,1,0] op_sel_hi:[0,0,1]
	v_sub_f32_e32 v96, v42, v25
	v_sub_f32_e32 v98, v41, v26
	v_sub_f32_e32 v100, v44, v27
	v_sub_f32_e32 v102, v43, v28
	v_sub_f32_e32 v97, v46, v29
	v_sub_f32_e32 v99, v45, v30
	v_sub_f32_e32 v101, v42, v33
	v_sub_f32_e32 v103, v41, v34
	v_fma_f32 v96, -v96, v96, s26
	v_fma_f32 v98, -v98, v98, s26
	v_fma_f32 v100, -v100, v100, s26
	v_fma_f32 v102, -v102, v102, s26
	v_fma_f32 v97, -v97, v97, s26
	v_fma_f32 v99, -v99, v99, s26
	v_fma_f32 v101, -v101, v101, s24
	v_fma_f32 v103, -v103, v103, s24
	v_exp_f32_e32 v96, v96
	v_exp_f32_e32 v98, v98
	v_exp_f32_e32 v100, v100
	v_exp_f32_e32 v102, v102
	v_exp_f32_e32 v97, v97
	v_exp_f32_e32 v99, v99
	v_exp_f32_e32 v101, v101
	v_exp_f32_e32 v103, v103
	v_pk_add_f32 v[88:89], v[88:89], v[104:105]
	v_pk_fma_f32 v[92:93], v[104:105], v[40:41], v[92:93]
	v_pk_add_f32 v[90:91], v[90:91], v[106:107]
	v_pk_add_f32 v[88:89], v[88:89], v[106:107]
	v_pk_fma_f32 v[92:93], v[106:107], v[44:45], v[92:93]
	v_pk_fma_f32 v[94:95], v[106:107], v[42:43], v[94:95]
	v_pk_add_f32 v[90:91], v[90:91], v[108:109]
	v_pk_fma_f32 v[94:95], v[108:109], v[46:47], v[94:95]
	v_sub_f32_e32 v108, v44, v35
	v_sub_f32_e32 v110, v43, v36
	v_sub_f32_e32 v105, v46, v37
	v_sub_f32_e32 v107, v45, v38
	v_sub_f32_e32 v109, v42, v41
	v_sub_f32_e32 v104, v43, v42
	v_sub_f32_e32 v111, v44, v43
	v_sub_f32_e32 v106, v45, v44
	v_fma_f32 v108, -v108, v108, s24
	v_fma_f32 v110, -v110, v110, s24
	v_fma_f32 v105, -v105, v105, s24
	v_fma_f32 v107, -v107, v107, s24
	v_fma_f32 v109, -v109, v109, s20
	v_fma_f32 v104, -v104, v104, s20
	v_fma_f32 v111, -v111, v111, s20
	v_fma_f32 v106, -v106, v106, s20
	v_exp_f32_e32 v108, v108
	v_exp_f32_e32 v110, v110
	v_exp_f32_e32 v105, v105
	v_exp_f32_e32 v107, v107
	v_exp_f32_e32 v109, v109
	v_exp_f32_e32 v104, v104
	v_exp_f32_e32 v111, v111
	v_exp_f32_e32 v106, v106
	v_add_f32_e32 v88, v88, v96
	v_fmac_f32_e32 v92, v96, v25
	v_add_f32_e32 v72, v72, v98
	v_fmac_f32_e32 v76, v98, v41
	v_add_f32_e32 v73, v73, v100
	v_fmac_f32_e32 v77, v100, v44
	v_add_f32_e32 v90, v90, v100
	v_fmac_f32_e32 v94, v100, v27
	v_add_f32_e32 v74, v74, v102
	v_fmac_f32_e32 v78, v102, v43
	v_add_f32_e32 v89, v89, v102
	v_fmac_f32_e32 v93, v102, v28
	v_add_f32_e32 v75, v75, v97
	v_fmac_f32_e32 v79, v97, v46
	v_add_f32_e32 v91, v91, v99
	v_fmac_f32_e32 v95, v99, v30
	v_add_f32_e32 v88, v88, v101
	v_fmac_f32_e32 v92, v101, v33
	v_add_f32_e32 v80, v80, v103
	v_fmac_f32_e32 v84, v103, v41
	v_sub_f32_e32 v96, v46, v45
	s_nop 0
	v_fma_f32 v96, -v96, v96, s20
	s_nop 0
	v_exp_f32_e32 v96, v96
	v_add_f32_e32 v81, v81, v108
	v_fmac_f32_e32 v85, v108, v44
	v_add_f32_e32 v90, v90, v108
	v_fmac_f32_e32 v94, v108, v35
	v_add_f32_e32 v82, v82, v110
	v_fmac_f32_e32 v86, v110, v43
	v_add_f32_e32 v89, v89, v110
	v_fmac_f32_e32 v93, v110, v36
	v_add_f32_e32 v83, v83, v105
	v_fmac_f32_e32 v87, v105, v46
	v_add_f32_e32 v91, v91, v107
	v_fmac_f32_e32 v95, v107, v38
	v_add_f32_e32 v88, v88, v109
	v_fmac_f32_e32 v92, v109, v41
	v_add_f32_e32 v89, v89, v111
	v_fmac_f32_e32 v93, v111, v44
	v_add_f32_e32 v90, v90, v111
	v_fmac_f32_e32 v94, v111, v43
	v_pk_add_f32 v[88:89], v[88:89], v[104:105] op_sel_hi:[1,0]
	v_pk_fma_f32 v[92:93], v[104:105], v[42:43], v[92:93] op_sel:[0,1,0] op_sel_hi:[0,0,1]
	v_pk_add_f32 v[90:91], v[90:91], v[106:107] op_sel_hi:[1,0]
	v_pk_fma_f32 v[94:95], v[106:107], v[44:45], v[94:95] op_sel:[0,1,0] op_sel_hi:[0,0,1]
	s_nop 0
	v_add_f32_e32 v91, v91, v96
	v_fmac_f32_e32 v95, v96, v46
	v_rcp_f32_e32 v96, v72
	v_rcp_f32_e32 v97, v73
	v_rcp_f32_e32 v98, v74
	v_rcp_f32_e32 v99, v75
	s_nop 0
	v_pk_mul_f32 v[76:77], v[76:77], s[34:35]
	v_pk_mul_f32 v[78:79], v[78:79], s[34:35]
	v_pk_mul_f32 v[76:77], v[76:77], v[96:97]
	v_pk_mul_f32 v[78:79], v[78:79], v[98:99]
	s_nop 0
	s_nop 0
	buffer_store_dwordx4 v[76:79], v114, s[12:15], 0 offen offset:2048 sc1
	s_waitcnt vmcnt(5)
	s_nop 0
	v_mov_b32_dpp v48, v52 row_shr:1 row_mask:0xf bank_mask:0xf
	v_mov_b32_dpp v49, v53 row_shr:1 row_mask:0xf bank_mask:0xf
	v_mov_b32_dpp v54, v50 row_shl:1 row_mask:0xf bank_mask:0xf
	v_mov_b32_dpp v55, v51 row_shl:1 row_mask:0xf bank_mask:0xf
	v_pk_mul_f32 v[50:51], v[50:51], s[32:33]
	v_pk_mul_f32 v[52:53], v[52:53], s[32:33]
	v_cndmask_b32_e64 v49, v49, v48, vcc
	v_cndmask_b32_e64 v54, v54, v55, s[16:17]
	v_pk_mul_f32 v[48:49], v[48:49], s[32:33]
	v_pk_mul_f32 v[54:55], v[54:55], s[32:33]
	s_setprio 0
	s_nop 0
	v_pk_add_f32 v[96:97], v[48:49], v[34:35] neg_lo:[0,1] neg_hi:[0,1]
	v_pk_add_f32 v[98:99], v[50:51], v[34:35] neg_lo:[0,1] neg_hi:[0,1]
	v_pk_add_f32 v[100:101], v[52:53], v[34:35] neg_lo:[0,1] neg_hi:[0,1]
	v_pk_add_f32 v[102:103], v[50:51], v[36:37] neg_lo:[0,1] neg_hi:[0,1]
	v_pk_fma_f32 v[96:97], v[96:97], v[96:97], s[28:29] neg_lo:[1,0,0] neg_hi:[1,0,0]
	v_pk_fma_f32 v[98:99], v[98:99], v[98:99], s[22:23] neg_lo:[1,0,0] neg_hi:[1,0,0]
	v_pk_fma_f32 v[100:101], v[100:101], v[100:101], s[28:29] neg_lo:[1,0,0] neg_hi:[1,0,0]
	v_pk_fma_f32 v[102:103], v[102:103], v[102:103], s[28:29] neg_lo:[1,0,0] neg_hi:[1,0,0]
	v_exp_f32_e32 v96, v96
	v_exp_f32_e32 v97, v97
	v_exp_f32_e32 v98, v98
	v_exp_f32_e32 v99, v99
	v_exp_f32_e32 v100, v100
	v_exp_f32_e32 v101, v101
	v_exp_f32_e32 v102, v102
	v_exp_f32_e32 v103, v103
	v_pk_add_f32 v[104:105], v[52:53], v[36:37] neg_lo:[0,1] neg_hi:[0,1]
	v_pk_add_f32 v[106:107], v[54:55], v[36:37] neg_lo:[0,1] neg_hi:[0,1]
	v_pk_add_f32 v[108:109], v[50:51], v[34:35] op_sel:[1,0] op_sel_hi:[0,1] neg_lo:[0,1] neg_hi:[0,1]
	v_pk_add_f32 v[110:111], v[52:53], v[36:37] op_sel:[1,0] op_sel_hi:[0,1] neg_lo:[0,1] neg_hi:[0,1]
	v_pk_fma_f32 v[104:105], v[104:105], v[104:105], s[22:23] neg_lo:[1,0,0] neg_hi:[1,0,0]
	v_pk_fma_f32 v[106:107], v[106:107], v[106:107], s[28:29] neg_lo:[1,0,0] neg_hi:[1,0,0]
	v_pk_fma_f32 v[108:109], v[108:109], v[108:109], s[26:27] neg_lo:[1,0,0] neg_hi:[1,0,0]
	v_pk_fma_f32 v[110:111], v[110:111], v[110:111], s[26:27] neg_lo:[1,0,0] neg_hi:[1,0,0]
	v_exp_f32_e32 v104, v104
	v_exp_f32_e32 v105, v105
	v_exp_f32_e32 v106, v106
	v_exp_f32_e32 v107, v107
	v_exp_f32_e32 v108, v108
	v_exp_f32_e32 v109, v109
	v_exp_f32_e32 v110, v110
	v_exp_f32_e32 v111, v111
	v_pk_add_f32 v[80:81], v[80:81], v[96:97]
	v_pk_fma_f32 v[84:85], v[96:97], v[48:49], v[84:85]
	v_pk_add_f32 v[82:83], v[82:83], v[102:103]
	v_pk_add_f32 v[80:81], v[80:81], v[98:99]
	v_pk_fma_f32 v[84:85], v[98:99], v[50:51], v[84:85]
	v_pk_fma_f32 v[86:87], v[102:103], v[50:51], v[86:87]
	v_pk_add_f32 v[80:81], v[80:81], v[100:101]
	v_pk_fma_f32 v[84:85], v[100:101], v[52:53], v[84:85]
	v_pk_add_f32 v[96:97], v[48:49], v[42:43] neg_lo:[0,1] neg_hi:[0,1]
	v_pk_add_f32 v[98:99], v[50:51], v[42:43] neg_lo:[0,1] neg_hi:[0,1]
	v_pk_add_f32 v[100:101], v[52:53], v[42:43] neg_lo:[0,1] neg_hi:[0,1]
	v_pk_add_f32 v[102:103], v[50:51], v[44:45] neg_lo:[0,1] neg_hi:[0,1]
	v_pk_fma_f32 v[96:97], v[96:97], v[96:97], s[26:27] neg_lo:[1,0,0] neg_hi:[1,0,0]
	v_pk_fma_f32 v[98:99], v[98:99], v[98:99], s[20:21] neg_lo:[1,0,0] neg_hi:[1,0,0]
	v_pk_fma_f32 v[100:101], v[100:101], v[100:101], s[26:27] neg_lo:[1,0,0] neg_hi:[1,0,0]
	v_pk_fma_f32 v[102:103], v[102:103], v[102:103], s[26:27] neg_lo:[1,0,0] neg_hi:[1,0,0]
	v_exp_f32_e32 v96, v96
	v_exp_f32_e32 v97, v97
	v_exp_f32_e32 v98, v98
	v_exp_f32_e32 v99, v99
	v_exp_f32_e32 v100, v100
	v_exp_f32_e32 v101, v101
	v_exp_f32_e32 v102, v102
	v_exp_f32_e32 v103, v103
	v_pk_add_f32 v[82:83], v[82:83], v[104:105]
	v_pk_fma_f32 v[86:87], v[104:105], v[52:53], v[86:87]
	v_pk_add_f32 v[80:81], v[80:81], v[108:109]
	v_pk_add_f32 v[82:83], v[82:83], v[106:107]
	v_pk_fma_f32 v[86:87], v[106:107], v[54:55], v[86:87]
	v_pk_fma_f32 v[84:85], v[108:109], v[50:51], v[84:85] op_sel:[0,1,0] op_sel_hi:[1,0,1]
	v_pk_add_f32 v[82:83], v[82:83], v[110:111]
	v_pk_fma_f32 v[86:87], v[110:111], v[52:53], v[86:87] op_sel:[0,1,0] op_sel_hi:[1,0,1]
	v_pk_add_f32 v[104:105], v[52:53], v[44:45] neg_lo:[0,1] neg_hi:[0,1]
	v_pk_add_f32 v[106:107], v[54:55], v[44:45] neg_lo:[0,1] neg_hi:[0,1]
	v_pk_add_f32 v[108:109], v[50:51], v[42:43] op_sel:[1,0] op_sel_hi:[0,1] neg_lo:[0,1] neg_hi:[0,1]
	v_pk_add_f32 v[110:111], v[52:53], v[44:45] op_sel:[1,0] op_sel_hi:[0,1] neg_lo:[0,1] neg_hi:[0,1]
	v_pk_fma_f32 v[104:105], v[104:105], v[104:105], s[20:21] neg_lo:[1,0,0] neg_hi:[1,0,0]
	v_pk_fma_f32 v[106:107], v[106:107], v[106:107], s[26:27] neg_lo:[1,0,0] neg_hi:[1,0,0]
	v_pk_fma_f32 v[108:109], v[108:109], v[108:109], s[24:25] neg_lo:[1,0,0] neg_hi:[1,0,0]
	v_pk_fma_f32 v[110:111], v[110:111], v[110:111], s[24:25] neg_lo:[1,0,0] neg_hi:[1,0,0]
	v_exp_f32_e32 v104, v104
	v_exp_f32_e32 v105, v105
	v_exp_f32_e32 v106, v106
	v_exp_f32_e32 v107, v107
	v_exp_f32_e32 v108, v108
	v_exp_f32_e32 v109, v109
	v_exp_f32_e32 v110, v110
	v_exp_f32_e32 v111, v111
	v_pk_add_f32 v[88:89], v[88:89], v[96:97]
	v_pk_fma_f32 v[92:93], v[96:97], v[48:49], v[92:93]
	v_pk_add_f32 v[90:91], v[90:91], v[102:103]
	v_pk_add_f32 v[88:89], v[88:89], v[98:99]
	v_pk_fma_f32 v[92:93], v[98:99], v[50:51], v[92:93]
	v_pk_fma_f32 v[94:95], v[102:103], v[50:51], v[94:95]
	v_pk_add_f32 v[88:89], v[88:89], v[100:101]
	v_pk_fma_f32 v[92:93], v[100:101], v[52:53], v[92:93]
	v_sub_f32_e32 v96, v49, v34
	v_sub_f32_e32 v98, v52, v35
	v_sub_f32_e32 v100, v51, v36
	v_sub_f32_e32 v102, v54, v37
	v_sub_f32_e32 v97, v49, v42
	v_sub_f32_e32 v99, v52, v43
	v_sub_f32_e32 v101, v51, v44
	v_sub_f32_e32 v103, v54, v45
	v_fma_f32 v96, -v96, v96, s26
	v_fma_f32 v98, -v98, v98, s26
	v_fma_f32 v100, -v100, v100, s26
	v_fma_f32 v102, -v102, v102, s26
	v_fma_f32 v97, -v97, v97, s24
	v_fma_f32 v99, -v99, v99, s24
	v_fma_f32 v101, -v101, v101, s24
	v_fma_f32 v103, -v103, v103, s24
	v_exp_f32_e32 v96, v96
	v_exp_f32_e32 v98, v98
	v_exp_f32_e32 v100, v100
	v_exp_f32_e32 v102, v102
	v_exp_f32_e32 v97, v97
	v_exp_f32_e32 v99, v99
	v_exp_f32_e32 v101, v101
	v_exp_f32_e32 v103, v103
	v_pk_add_f32 v[90:91], v[90:91], v[104:105]
	v_pk_fma_f32 v[94:95], v[104:105], v[52:53], v[94:95]
	v_pk_add_f32 v[88:89], v[88:89], v[108:109]
	v_pk_add_f32 v[90:91], v[90:91], v[106:107]
	v_pk_fma_f32 v[94:95], v[106:107], v[54:55], v[94:95]
	v_pk_fma_f32 v[92:93], v[108:109], v[50:51], v[92:93] op_sel:[0,1,0] op_sel_hi:[1,0,1]
	v_pk_add_f32 v[90:91], v[90:91], v[110:111]
	v_pk_fma_f32 v[94:95], v[110:111], v[52:53], v[94:95] op_sel:[0,1,0] op_sel_hi:[1,0,1]
	v_add_f32_e32 v80, v80, v96
	v_fmac_f32_e32 v84, v96, v49
	v_add_f32_e32 v81, v81, v98
	v_fmac_f32_e32 v85, v98, v52
	v_add_f32_e32 v82, v82, v100
	v_fmac_f32_e32 v86, v100, v51
	v_add_f32_e32 v83, v83, v102
	v_fmac_f32_e32 v87, v102, v54
	v_add_f32_e32 v88, v88, v97
	v_fmac_f32_e32 v92, v97, v49
	v_add_f32_e32 v89, v89, v99
	v_fmac_f32_e32 v93, v99, v52
	v_add_f32_e32 v90, v90, v101
	v_fmac_f32_e32 v94, v101, v51
	v_add_f32_e32 v91, v91, v103
	v_fmac_f32_e32 v95, v103, v54
	v_rcp_f32_e32 v96, v80
	v_rcp_f32_e32 v97, v81
	v_rcp_f32_e32 v98, v82
	v_rcp_f32_e32 v99, v83
	v_pk_mul_f32 v[84:85], v[84:85], s[34:35]
	v_pk_mul_f32 v[86:87], v[86:87], s[34:35]
	v_pk_mul_f32 v[84:85], v[84:85], v[96:97]
	v_pk_mul_f32 v[86:87], v[86:87], v[98:99]
	s_nop 0
	s_nop 0
	buffer_store_dwordx4 v[84:87], v119, s[12:15], 0 offen sc1
	s_waitcnt vmcnt(3)
	s_nop 0
	v_mov_b32_dpp v56, v60 row_shr:1 row_mask:0xf bank_mask:0xf
	v_mov_b32_dpp v57, v61 row_shr:1 row_mask:0xf bank_mask:0xf
	v_mov_b32_dpp v62, v58 row_shl:1 row_mask:0xf bank_mask:0xf
	v_mov_b32_dpp v63, v59 row_shl:1 row_mask:0xf bank_mask:0xf
	v_pk_mul_f32 v[58:59], v[58:59], s[32:33]
	v_pk_mul_f32 v[60:61], v[60:61], s[32:33]
	v_cndmask_b32_e64 v57, v57, v56, vcc
	v_cndmask_b32_e64 v62, v62, v63, s[16:17]
	v_pk_mul_f32 v[56:57], v[56:57], s[32:33]
	v_pk_mul_f32 v[62:63], v[62:63], s[32:33]
	s_setprio 0
	s_nop 0
	v_pk_add_f32 v[96:97], v[56:57], v[42:43] neg_lo:[0,1] neg_hi:[0,1]
	v_pk_add_f32 v[98:99], v[58:59], v[42:43] neg_lo:[0,1] neg_hi:[0,1]
	v_pk_add_f32 v[100:101], v[60:61], v[42:43] neg_lo:[0,1] neg_hi:[0,1]
	v_pk_add_f32 v[102:103], v[58:59], v[44:45] neg_lo:[0,1] neg_hi:[0,1]
	v_pk_fma_f32 v[96:97], v[96:97], v[96:97], s[28:29] neg_lo:[1,0,0] neg_hi:[1,0,0]
	v_pk_fma_f32 v[98:99], v[98:99], v[98:99], s[22:23] neg_lo:[1,0,0] neg_hi:[1,0,0]
	v_pk_fma_f32 v[100:101], v[100:101], v[100:101], s[28:29] neg_lo:[1,0,0] neg_hi:[1,0,0]
	v_pk_fma_f32 v[102:103], v[102:103], v[102:103], s[28:29] neg_lo:[1,0,0] neg_hi:[1,0,0]
	v_exp_f32_e32 v96, v96
	v_exp_f32_e32 v97, v97
	v_exp_f32_e32 v98, v98
	v_exp_f32_e32 v99, v99
	v_exp_f32_e32 v100, v100
	v_exp_f32_e32 v101, v101
	v_exp_f32_e32 v102, v102
	v_exp_f32_e32 v103, v103
	v_pk_add_f32 v[104:105], v[60:61], v[44:45] neg_lo:[0,1] neg_hi:[0,1]
	v_pk_add_f32 v[106:107], v[62:63], v[44:45] neg_lo:[0,1] neg_hi:[0,1]
	v_pk_add_f32 v[108:109], v[58:59], v[42:43] op_sel:[1,0] op_sel_hi:[0,1] neg_lo:[0,1] neg_hi:[0,1]
	v_pk_add_f32 v[110:111], v[60:61], v[44:45] op_sel:[1,0] op_sel_hi:[0,1] neg_lo:[0,1] neg_hi:[0,1]
	v_pk_fma_f32 v[104:105], v[104:105], v[104:105], s[22:23] neg_lo:[1,0,0] neg_hi:[1,0,0]
	v_pk_fma_f32 v[106:107], v[106:107], v[106:107], s[28:29] neg_lo:[1,0,0] neg_hi:[1,0,0]
	v_pk_fma_f32 v[108:109], v[108:109], v[108:109], s[26:27] neg_lo:[1,0,0] neg_hi:[1,0,0]
	v_pk_fma_f32 v[110:111], v[110:111], v[110:111], s[26:27] neg_lo:[1,0,0] neg_hi:[1,0,0]
	v_exp_f32_e32 v104, v104
	v_exp_f32_e32 v105, v105
	v_exp_f32_e32 v106, v106
	v_exp_f32_e32 v107, v107
	v_exp_f32_e32 v108, v108
	v_exp_f32_e32 v109, v109
	v_exp_f32_e32 v110, v110
	v_exp_f32_e32 v111, v111
	v_pk_add_f32 v[88:89], v[88:89], v[96:97]
	v_pk_fma_f32 v[92:93], v[96:97], v[56:57], v[92:93]
	v_pk_add_f32 v[90:91], v[90:91], v[102:103]
	v_pk_add_f32 v[88:89], v[88:89], v[98:99]
	v_pk_fma_f32 v[92:93], v[98:99], v[58:59], v[92:93]
	v_pk_fma_f32 v[94:95], v[102:103], v[58:59], v[94:95]
	v_pk_add_f32 v[88:89], v[88:89], v[100:101]
	v_pk_fma_f32 v[92:93], v[100:101], v[60:61], v[92:93]
	v_sub_f32_e32 v96, v57, v42
	v_sub_f32_e32 v98, v60, v43
	v_sub_f32_e32 v100, v59, v44
	v_sub_f32_e32 v102, v62, v45
	v_fma_f32 v96, -v96, v96, s26
	v_fma_f32 v98, -v98, v98, s26
	v_fma_f32 v100, -v100, v100, s26
	v_fma_f32 v102, -v102, v102, s26
	v_exp_f32_e32 v96, v96
	v_exp_f32_e32 v98, v98
	v_exp_f32_e32 v100, v100
	v_exp_f32_e32 v102, v102
	v_pk_add_f32 v[90:91], v[90:91], v[104:105]
	v_pk_fma_f32 v[94:95], v[104:105], v[60:61], v[94:95]
	v_pk_add_f32 v[88:89], v[88:89], v[108:109]
	v_pk_add_f32 v[90:91], v[90:91], v[106:107]
	v_pk_fma_f32 v[94:95], v[106:107], v[62:63], v[94:95]
	v_pk_fma_f32 v[92:93], v[108:109], v[58:59], v[92:93] op_sel:[0,1,0] op_sel_hi:[1,0,1]
	v_pk_add_f32 v[90:91], v[90:91], v[110:111]
	v_pk_fma_f32 v[94:95], v[110:111], v[60:61], v[94:95] op_sel:[0,1,0] op_sel_hi:[1,0,1]
	v_add_f32_e32 v88, v88, v96
	v_fmac_f32_e32 v92, v96, v57
	v_add_f32_e32 v89, v89, v98
	v_fmac_f32_e32 v93, v98, v60
	v_add_f32_e32 v90, v90, v100
	v_fmac_f32_e32 v94, v100, v59
	v_add_f32_e32 v91, v91, v102
	v_fmac_f32_e32 v95, v102, v62
	v_rcp_f32_e32 v96, v88
	v_rcp_f32_e32 v97, v89
	v_rcp_f32_e32 v98, v90
	v_rcp_f32_e32 v99, v91
	v_pk_mul_f32 v[92:93], v[92:93], s[34:35]
	v_pk_mul_f32 v[94:95], v[94:95], s[34:35]
	v_pk_mul_f32 v[92:93], v[92:93], v[96:97]
	v_pk_mul_f32 v[94:95], v[94:95], v[98:99]
	s_nop 0
	s_nop 0
	buffer_store_dwordx4 v[92:95], v119, s[12:15], 0 offen offset:2048 sc1
	s_endpgm

	.amdhsa_kernel _Z16bilateral_kernelPKfS0_Pf
		.amdhsa_group_segment_fixed_size 0
		.amdhsa_private_segment_fixed_size 0
		.amdhsa_kernarg_size 24
		.amdhsa_user_sgpr_count 2
		.amdhsa_user_sgpr_dispatch_ptr 0
		.amdhsa_user_sgpr_queue_ptr 0
		.amdhsa_user_sgpr_kernarg_segment_ptr 1
		.amdhsa_user_sgpr_dispatch_id 0
		.amdhsa_user_sgpr_kernarg_preload_length 0
		.amdhsa_user_sgpr_kernarg_preload_offset 0
		.amdhsa_user_sgpr_private_segment_size 0
		.amdhsa_uses_dynamic_stack 0
		.amdhsa_enable_private_segment 0
		.amdhsa_system_sgpr_workgroup_id_x 1
		.amdhsa_system_sgpr_workgroup_id_y 0
		.amdhsa_system_sgpr_workgroup_id_z 0
		.amdhsa_system_sgpr_workgroup_info 0
		.amdhsa_system_vgpr_workitem_id 0
		.amdhsa_next_free_vgpr 144
		.amdhsa_next_free_sgpr 40
		.amdhsa_accum_offset 144
		.amdhsa_reserve_vcc 1
		.amdhsa_float_round_mode_32 0
		.amdhsa_float_round_mode_16_64 0
		.amdhsa_float_denorm_mode_32 3
		.amdhsa_float_denorm_mode_16_64 3
		.amdhsa_dx10_clamp 1
		.amdhsa_ieee_mode 1
		.amdhsa_fp16_overflow 0
		.amdhsa_tg_split 0
		.amdhsa_exception_fp_ieee_invalid_op 0
		.amdhsa_exception_fp_denorm_src 0
		.amdhsa_exception_fp_ieee_div_zero 0
		.amdhsa_exception_fp_ieee_overflow 0
		.amdhsa_exception_fp_ieee_underflow 0
		.amdhsa_exception_fp_ieee_inexact 0
		.amdhsa_exception_int_div_zero 0
	.end_amdhsa_kernel

amdhsa.kernels:
  - .agpr_count:     0
    .args:
      - .actual_access:  read_only
        .address_space:  global
        .offset:         0
        .size:           8
        .value_kind:     global_buffer
      - .actual_access:  read_only
        .address_space:  global
        .offset:         8
        .size:           8
        .value_kind:     global_buffer
      - .actual_access:  write_only
        .address_space:  global
        .offset:         16
        .size:           8
        .value_kind:     global_buffer
    .group_segment_fixed_size: 0
    .kernarg_segment_align: 8
    .kernarg_segment_size: 24
    .language:       OpenCL C
    .language_version:
      - 2
      - 0
    .max_flat_workgroup_size: 256
    .name:           _Z16bilateral_kernelPKfS0_Pf
    .private_segment_fixed_size: 0
    .sgpr_count:     46
    .sgpr_spill_count: 0
    .symbol:         _Z16bilateral_kernelPKfS0_Pf.kd
    .uniform_work_group_size: 1
    .uses_dynamic_stack: false
    .vgpr_count:     144
    .vgpr_spill_count: 0
    .wavefront_size: 64
